# fp8 GEMM K-loops: accumulators of the second sub-phase zeroed in the MFMA gaps of the first K iteration (out-of-line copy of the first 16 MFMAs) instead of in the tile header
# speedup vs baseline: 1.0042x; 1.0042x over previous
.LBB0_545:
	s_ashr_i32 s15, s14, 31
	s_lshl_b64 s[16:17], s[14:15], 18
	s_add_u32 s16, s30, s16
	s_addc_u32 s17, s31, s17
	s_and_b64 s[18:19], s[2:3], exec
	s_cselect_b32 s1, s17, s25
	s_cselect_b32 s15, s16, s24
	s_ashr_i32 s13, s12, 31
	s_lshl_b64 s[18:19], s[12:13], 18
	s_add_u32 s18, s34, s18
	s_addc_u32 s19, s35, s19
	s_and_b64 s[26:27], s[2:3], exec
	s_cselect_b32 s13, s19, s23
	s_cselect_b32 s33, s18, s22
	s_add_u32 s59, s22, 0x100
	s_addc_u32 s60, s23, 0
	s_add_u32 s22, s24, 0x80
	v_mov_b32_e32 v2, 0
	s_addc_u32 s23, s25, 0
	s_mov_b32 s61, -2
	v_mov_b32_e32 v3, v2
	s_waitcnt vmcnt(0)
	v_mov_b64_e32 v[66:67], v[2:3]
	v_mov_b64_e32 v[68:69], v[2:3]
	v_mov_b64_e32 v[70:71], v[2:3]
	v_mov_b64_e32 v[72:73], v[2:3]
	v_mov_b64_e32 v[78:79], v[2:3]
	v_mov_b64_e32 v[80:81], v[2:3]
	v_mov_b64_e32 v[86:87], v[2:3]
	v_mov_b64_e32 v[88:89], v[2:3]
	v_mov_b64_e32 v[94:95], v[2:3]
	v_mov_b64_e32 v[96:97], v[2:3]
	v_mov_b64_e32 v[102:103], v[2:3]
	v_mov_b64_e32 v[104:105], v[2:3]
	v_mov_b64_e32 v[114:115], v[2:3]
	v_mov_b64_e32 v[116:117], v[2:3]
	v_mov_b64_e32 v[118:119], v[2:3]
	v_mov_b64_e32 v[120:121], v[2:3]
	v_mov_b64_e32 v[74:75], v[2:3]
	v_mov_b64_e32 v[76:77], v[2:3]
	v_mov_b64_e32 v[82:83], v[2:3]
	v_mov_b64_e32 v[84:85], v[2:3]
	v_mov_b64_e32 v[90:91], v[2:3]
	v_mov_b64_e32 v[92:93], v[2:3]
	v_mov_b64_e32 v[98:99], v[2:3]
	v_mov_b64_e32 v[100:101], v[2:3]
	v_mov_b64_e32 v[106:107], v[2:3]
	v_mov_b64_e32 v[108:109], v[2:3]
	v_mov_b64_e32 v[110:111], v[2:3]
	v_mov_b64_e32 v[112:113], v[2:3]
	v_mov_b64_e32 v[122:123], v[2:3]
	v_mov_b64_e32 v[124:125], v[2:3]
	v_mov_b64_e32 v[126:127], v[2:3]
	v_mov_b64_e32 v[128:129], v[2:3]
	s_branch .LBB0_546
.Llzf_2:
	v_mfma_f32_16x16x128_f8f6f4 v[126:129], v[130:137], v[186:193], v[126:129]
	v_mov_b32_e32 v4, 0
	v_mov_b32_e32 v5, 0
	v_mov_b32_e32 v6, 0
	v_mov_b32_e32 v7, 0
	v_mfma_f32_16x16x128_f8f6f4 v[122:125], v[138:145], v[186:193], v[122:125]
	v_mov_b32_e32 v8, 0
	v_mov_b32_e32 v9, 0
	v_mov_b32_e32 v14, 0
	v_mov_b32_e32 v15, 0
	v_mfma_f32_16x16x128_f8f6f4 v[110:113], v[130:137], v[194:201], v[110:113]
	v_mov_b32_e32 v16, 0
	v_mov_b32_e32 v17, 0
	v_mov_b32_e32 v22, 0
	v_mov_b32_e32 v23, 0
	v_mfma_f32_16x16x128_f8f6f4 v[106:109], v[138:145], v[194:201], v[106:109]
	v_mov_b32_e32 v24, 0
	v_mov_b32_e32 v25, 0
	v_mov_b32_e32 v30, 0
	v_mov_b32_e32 v31, 0
	v_mfma_f32_16x16x128_f8f6f4 v[98:101], v[130:137], v[202:209], v[98:101]
	v_mov_b32_e32 v32, 0
	v_mov_b32_e32 v33, 0
	v_mov_b32_e32 v38, 0
	v_mov_b32_e32 v39, 0
	v_mfma_f32_16x16x128_f8f6f4 v[162:165], v[138:145], v[202:209], v[90:93]
	v_mov_b32_e32 v40, 0
	v_mov_b32_e32 v41, 0
	v_mov_b32_e32 v46, 0
	v_mov_b32_e32 v47, 0
	v_mfma_f32_16x16x128_f8f6f4 v[172:175], v[130:137], v[210:217], v[82:85]
	v_mov_b32_e32 v48, 0
	v_mov_b32_e32 v49, 0
	v_mov_b32_e32 v54, 0
	v_mov_b32_e32 v55, 0
	v_mfma_f32_16x16x128_f8f6f4 v[218:221], v[138:145], v[210:217], v[74:77]
	v_mov_b32_e32 v56, 0
	v_mov_b32_e32 v57, 0
	v_mov_b32_e32 v10, 0
	v_mov_b32_e32 v11, 0
	s_setprio 0
	s_setprio 1
	v_mfma_f32_16x16x128_f8f6f4 v[118:121], v[146:153], v[186:193], v[118:121]
	v_mov_b32_e32 v12, 0
	v_mov_b32_e32 v13, 0
	v_mov_b32_e32 v18, 0
	v_mov_b32_e32 v19, 0
	v_mfma_f32_16x16x128_f8f6f4 v[114:117], v[154:161], v[186:193], v[114:117]
	v_mov_b32_e32 v20, 0
	v_mov_b32_e32 v21, 0
	v_mov_b32_e32 v26, 0
	v_mov_b32_e32 v27, 0
	v_mfma_f32_16x16x128_f8f6f4 v[102:105], v[146:153], v[194:201], v[102:105]
	v_mov_b32_e32 v28, 0
	v_mov_b32_e32 v29, 0
	v_mov_b32_e32 v34, 0
	v_mov_b32_e32 v35, 0
	v_mfma_f32_16x16x128_f8f6f4 v[186:189], v[154:161], v[194:201], v[94:97]
	v_mov_b32_e32 v36, 0
	v_mov_b32_e32 v37, 0
	v_mov_b32_e32 v42, 0
	v_mov_b32_e32 v43, 0
	v_mfma_f32_16x16x128_f8f6f4 v[190:193], v[146:153], v[202:209], v[86:89]
	v_mov_b32_e32 v44, 0
	v_mov_b32_e32 v45, 0
	v_mov_b32_e32 v50, 0
	v_mov_b32_e32 v51, 0
	v_mfma_f32_16x16x128_f8f6f4 v[194:197], v[154:161], v[202:209], v[78:81]
	v_mov_b32_e32 v52, 0
	v_mov_b32_e32 v53, 0
	v_mov_b32_e32 v58, 0
	v_mov_b32_e32 v59, 0
	v_mfma_f32_16x16x128_f8f6f4 v[198:201], v[146:153], v[210:217], v[70:73]
	v_mov_b32_e32 v60, 0
	v_mov_b32_e32 v61, 0
	v_mov_b32_e32 v62, 0
	v_mov_b32_e32 v63, 0
	v_mfma_f32_16x16x128_f8f6f4 v[202:205], v[154:161], v[210:217], v[66:69]
	v_mov_b32_e32 v64, 0
	v_mov_b32_e32 v65, 0
	s_branch .Llzj_2
.LBB0_546:
	v_add_u32_e32 v0, s21, v170
	ds_read_b128 v[130:133], v0
	ds_read_b128 v[134:137], v0 offset:1024
	ds_read_b128 v[138:141], v0 offset:2048
	ds_read_b128 v[142:145], v0 offset:3072
	v_add_u32_e32 v0, s39, v170
	ds_read_b128 v[146:149], v0
	ds_read_b128 v[150:153], v0 offset:1024
	ds_read_b128 v[154:157], v0 offset:2048
	ds_read_b128 v[158:161], v0 offset:3072
	s_add_u32 s24, s22, 0x80
	s_addc_u32 s25, s23, 0
	s_cmp_eq_u32 s61, 4
	s_cselect_b32 s25, s1, s25
	s_cselect_b32 s24, s15, s24
	s_cselect_b32 s27, s13, s60
	s_cselect_b32 s26, s33, s59
	v_mov_b32_e32 v0, v167
	ds_read_b128 v[186:189], v171
	ds_read_b128 v[190:193], v171 offset:1024
	ds_read_b128 v[194:197], v171 offset:2048
	ds_read_b128 v[198:201], v171 offset:3072
	ds_read_b128 v[202:205], v171 offset:4096
	ds_read_b128 v[206:209], v171 offset:5120
	ds_read_b128 v[210:213], v171 offset:6144
	ds_read_b128 v[214:217], v171 offset:7168
	s_add_i32 m0, s42, 0xc000
	v_add_u32_e32 v0, 0x20000, v0
	global_load_lds_dwordx4 v0, s[22:23]
	v_mov_b32_e32 v0, v169
	s_add_i32 m0, s42, 0xe000
	v_add_u32_e32 v0, 0x20000, v0
	global_load_lds_dwordx4 v0, s[22:23]
	s_waitcnt vmcnt(8)
	s_waitcnt lgkmcnt(0)
	s_barrier
	s_setprio 1
	s_waitcnt lgkmcnt(0)
	s_cmp_eq_u32 s61, -2
	s_cbranch_scc1 .Llzf_2
	v_mfma_f32_16x16x128_f8f6f4 v[126:129], v[130:137], v[186:193], v[126:129]
	v_mfma_f32_16x16x128_f8f6f4 v[122:125], v[138:145], v[186:193], v[122:125]
	v_mfma_f32_16x16x128_f8f6f4 v[110:113], v[130:137], v[194:201], v[110:113]
	v_mfma_f32_16x16x128_f8f6f4 v[106:109], v[138:145], v[194:201], v[106:109]
	v_mfma_f32_16x16x128_f8f6f4 v[98:101], v[130:137], v[202:209], v[98:101]
	v_mfma_f32_16x16x128_f8f6f4 v[162:165], v[138:145], v[202:209], v[90:93]
	v_mfma_f32_16x16x128_f8f6f4 v[172:175], v[130:137], v[210:217], v[82:85]
	v_mfma_f32_16x16x128_f8f6f4 v[218:221], v[138:145], v[210:217], v[74:77]
	s_setprio 0
	s_setprio 1
	v_mfma_f32_16x16x128_f8f6f4 v[118:121], v[146:153], v[186:193], v[118:121]
	v_mfma_f32_16x16x128_f8f6f4 v[114:117], v[154:161], v[186:193], v[114:117]
	v_mfma_f32_16x16x128_f8f6f4 v[102:105], v[146:153], v[194:201], v[102:105]
	v_mfma_f32_16x16x128_f8f6f4 v[186:189], v[154:161], v[194:201], v[94:97]
	v_mfma_f32_16x16x128_f8f6f4 v[190:193], v[146:153], v[202:209], v[86:89]
	v_mfma_f32_16x16x128_f8f6f4 v[194:197], v[154:161], v[202:209], v[78:81]
	v_mfma_f32_16x16x128_f8f6f4 v[198:201], v[146:153], v[210:217], v[70:73]
	v_mfma_f32_16x16x128_f8f6f4 v[202:205], v[154:161], v[210:217], v[66:69]
.Llzj_2:
	s_setprio 0
	s_barrier
	v_mov_b32_e32 v0, v166
	s_mov_b32 m0, s37
	s_nop 2
	ds_read_b128 v[66:69], v171 offset:16384
	ds_read_b128 v[70:73], v171 offset:17408
	ds_read_b128 v[74:77], v171 offset:18432
	ds_read_b128 v[78:81], v171 offset:19456
	ds_read_b128 v[82:85], v171 offset:20480
	ds_read_b128 v[86:89], v171 offset:21504
	ds_read_b128 v[90:93], v171 offset:22528
	ds_read_b128 v[94:97], v171 offset:23552
	s_add_u32 s62, s26, 0x20000
	global_load_lds_dwordx4 v0, s[26:27]
	v_mov_b32_e32 v0, v168
	s_mov_b32 m0, s38
	s_addc_u32 s63, s27, 0
	global_load_lds_dwordx4 v0, s[26:27]
	v_mov_b32_e32 v0, v166
	s_mov_b32 m0, s40
	s_nop 0
	global_load_lds_dwordx4 v0, s[62:63]
	v_mov_b32_e32 v0, v168
	s_mov_b32 m0, s41
	s_nop 0
	global_load_lds_dwordx4 v0, s[62:63]
	v_mov_b32_e32 v0, v167
	s_mov_b32 m0, s42
	s_nop 0
	global_load_lds_dwordx4 v0, s[24:25]
	v_mov_b32_e32 v0, v169
	s_mov_b32 m0, s43
	s_nop 0
	global_load_lds_dwordx4 v0, s[24:25]
	s_waitcnt vmcnt(8)
	s_waitcnt lgkmcnt(0)
	s_barrier
	s_setprio 1
	s_waitcnt lgkmcnt(0)
	v_mfma_f32_16x16x128_f8f6f4 v[62:65], v[130:137], v[66:73], v[62:65]
	v_mfma_f32_16x16x128_f8f6f4 v[58:61], v[138:145], v[66:73], v[58:61]
	v_mfma_f32_16x16x128_f8f6f4 v[50:53], v[130:137], v[74:81], v[50:53]
	v_mfma_f32_16x16x128_f8f6f4 v[206:209], v[138:145], v[74:81], v[42:45]
	v_mfma_f32_16x16x128_f8f6f4 v[210:213], v[130:137], v[82:89], v[34:37]
	v_mfma_f32_16x16x128_f8f6f4 v[214:217], v[138:145], v[82:89], v[26:29]
	v_mfma_f32_16x16x128_f8f6f4 v[244:247], v[130:137], v[90:97], v[18:21]
	v_mfma_f32_16x16x128_f8f6f4 v[248:251], v[138:145], v[90:97], v[10:13]
	s_setprio 0
	s_setprio 1
	v_mfma_f32_16x16x128_f8f6f4 v[54:57], v[146:153], v[66:73], v[54:57]
	v_mfma_f32_16x16x128_f8f6f4 v[234:237], v[154:161], v[66:73], v[46:49]
	v_mfma_f32_16x16x128_f8f6f4 v[176:179], v[146:153], v[74:81], v[38:41]
	v_mfma_f32_16x16x128_f8f6f4 v[180:183], v[154:161], v[74:81], v[30:33]
	v_mfma_f32_16x16x128_f8f6f4 v[226:229], v[146:153], v[82:89], v[22:25]
	v_mfma_f32_16x16x128_f8f6f4 v[230:233], v[154:161], v[82:89], v[14:17]
	v_mfma_f32_16x16x128_f8f6f4 v[222:225], v[146:153], v[90:97], v[6:9]
	v_mfma_f32_16x16x128_f8f6f4 v[238:241], v[154:161], v[90:97], v[2:5]
	s_setprio 0
	s_barrier
	v_add_u32_e32 v0, s48, v170
	s_nop 3
	ds_read_b128 v[2:5], v0
	ds_read_b128 v[6:9], v0 offset:1024
	ds_read_b128 v[10:13], v0 offset:2048
	ds_read_b128 v[14:17], v0 offset:3072
	v_add_u32_e32 v0, s53, v170
	ds_read_b128 v[130:133], v0
	ds_read_b128 v[134:137], v0 offset:1024
	ds_read_b128 v[138:141], v0 offset:2048
	ds_read_b128 v[142:145], v0 offset:3072
	v_mov_b32_e32 v0, v167
	ds_read_b128 v[18:21], v171 offset:32768
	ds_read_b128 v[22:25], v171 offset:33792
	ds_read_b128 v[26:29], v171 offset:34816
	ds_read_b128 v[30:33], v171 offset:35840
	ds_read_b128 v[34:37], v171 offset:36864
	ds_read_b128 v[38:41], v171 offset:37888
	ds_read_b128 v[42:45], v171 offset:38912
	ds_read_b128 v[46:49], v171 offset:39936
	s_mov_b32 m0, s44
	v_add_u32_e32 v0, 0x20000, v0
	global_load_lds_dwordx4 v0, s[24:25]
	v_mov_b32_e32 v0, v169
	s_mov_b32 m0, s45
	v_add_u32_e32 v0, 0x20000, v0
	global_load_lds_dwordx4 v0, s[24:25]
	s_waitcnt vmcnt(8)
	s_waitcnt lgkmcnt(0)
	s_barrier
	s_setprio 1
	s_waitcnt lgkmcnt(0)
	v_mfma_f32_16x16x128_f8f6f4 v[126:129], v[2:9], v[18:25], v[126:129]
	v_mfma_f32_16x16x128_f8f6f4 v[122:125], v[10:17], v[18:25], v[122:125]
	v_mfma_f32_16x16x128_f8f6f4 v[110:113], v[2:9], v[26:33], v[110:113]
	v_mfma_f32_16x16x128_f8f6f4 v[106:109], v[10:17], v[26:33], v[106:109]
	v_mfma_f32_16x16x128_f8f6f4 v[98:101], v[2:9], v[34:41], v[98:101]
	v_mfma_f32_16x16x128_f8f6f4 v[90:93], v[10:17], v[34:41], v[162:165]
	v_mfma_f32_16x16x128_f8f6f4 v[82:85], v[2:9], v[42:49], v[172:175]
	v_mfma_f32_16x16x128_f8f6f4 v[74:77], v[10:17], v[42:49], v[218:221]
	s_setprio 0
	s_setprio 1
	v_mfma_f32_16x16x128_f8f6f4 v[118:121], v[130:137], v[18:25], v[118:121]
	v_mfma_f32_16x16x128_f8f6f4 v[114:117], v[138:145], v[18:25], v[114:117]
	v_mfma_f32_16x16x128_f8f6f4 v[102:105], v[130:137], v[26:33], v[102:105]
	v_mfma_f32_16x16x128_f8f6f4 v[94:97], v[138:145], v[26:33], v[186:189]
	v_mfma_f32_16x16x128_f8f6f4 v[86:89], v[130:137], v[34:41], v[190:193]
	v_mfma_f32_16x16x128_f8f6f4 v[78:81], v[138:145], v[34:41], v[194:197]
	v_mfma_f32_16x16x128_f8f6f4 v[70:73], v[130:137], v[42:49], v[198:201]
	v_mfma_f32_16x16x128_f8f6f4 v[66:69], v[138:145], v[42:49], v[202:205]
	s_setprio 0
	s_barrier
	v_mov_b32_e32 v0, v166
	ds_read_b128 v[146:149], v171 offset:49152
	ds_read_b128 v[150:153], v171 offset:50176
	ds_read_b128 v[154:157], v171 offset:51200
	ds_read_b128 v[158:161], v171 offset:52224
	ds_read_b128 v[186:189], v171 offset:53248
	ds_read_b128 v[190:193], v171 offset:54272
	ds_read_b128 v[194:197], v171 offset:55296
	ds_read_b128 v[198:201], v171 offset:56320
	s_mov_b32 m0, s49
	v_lshl_add_u64 v[18:19], s[26:27], 0, v[0:1]
	v_lshl_add_u64 v[18:19], v[18:19], 0, s[82:83]
	v_mov_b32_e32 v0, v168
	global_load_lds_dwordx4 v[18:19], off
	s_mov_b32 m0, s50
	v_lshl_add_u64 v[18:19], s[26:27], 0, v[0:1]
	v_lshl_add_u64 v[18:19], v[18:19], 0, s[82:83]
	s_add_u32 s26, s26, 0x20080
	v_mov_b32_e32 v0, v166
	global_load_lds_dwordx4 v[18:19], off
	s_addc_u32 s27, s27, 0
	s_mov_b32 m0, s54
	s_nop 0
	global_load_lds_dwordx4 v0, s[26:27]
	v_mov_b32_e32 v0, v168
	s_mov_b32 m0, s55
	s_nop 0
	global_load_lds_dwordx4 v0, s[26:27]
	v_mov_b32_e32 v0, v167
	s_mov_b32 m0, s51
	v_lshl_add_u64 v[18:19], s[24:25], 0, v[0:1]
	v_lshl_add_u64 v[18:19], v[18:19], 0, s[82:83]
	v_mov_b32_e32 v0, v169
	global_load_lds_dwordx4 v[18:19], off
	s_mov_b32 m0, s52
	v_lshl_add_u64 v[18:19], s[24:25], 0, v[0:1]
	v_lshl_add_u64 v[18:19], v[18:19], 0, s[82:83]
	global_load_lds_dwordx4 v[18:19], off
	s_waitcnt vmcnt(8)
	s_waitcnt lgkmcnt(0)
	s_barrier
	s_setprio 1
	s_waitcnt lgkmcnt(0)
	v_mfma_f32_16x16x128_f8f6f4 v[62:65], v[2:9], v[146:153], v[62:65]
	v_mfma_f32_16x16x128_f8f6f4 v[58:61], v[10:17], v[146:153], v[58:61]
	v_mfma_f32_16x16x128_f8f6f4 v[50:53], v[2:9], v[154:161], v[50:53]
	v_mfma_f32_16x16x128_f8f6f4 v[42:45], v[10:17], v[154:161], v[206:209]
	v_mfma_f32_16x16x128_f8f6f4 v[34:37], v[2:9], v[186:193], v[210:213]
	v_mfma_f32_16x16x128_f8f6f4 v[26:29], v[10:17], v[186:193], v[214:217]
	v_mfma_f32_16x16x128_f8f6f4 v[18:21], v[2:9], v[194:201], v[244:247]
	v_mfma_f32_16x16x128_f8f6f4 v[10:13], v[10:17], v[194:201], v[248:251]
	s_setprio 0
	s_setprio 1
	v_mfma_f32_16x16x128_f8f6f4 v[54:57], v[130:137], v[146:153], v[54:57]
	v_mfma_f32_16x16x128_f8f6f4 v[46:49], v[138:145], v[146:153], v[234:237]
	v_mfma_f32_16x16x128_f8f6f4 v[38:41], v[130:137], v[154:161], v[176:179]
	v_mfma_f32_16x16x128_f8f6f4 v[30:33], v[138:145], v[154:161], v[180:183]
	v_mfma_f32_16x16x128_f8f6f4 v[22:25], v[130:137], v[186:193], v[226:229]
	v_mfma_f32_16x16x128_f8f6f4 v[14:17], v[138:145], v[186:193], v[230:233]
	v_mfma_f32_16x16x128_f8f6f4 v[6:9], v[130:137], v[194:201], v[222:225]
	v_mfma_f32_16x16x128_f8f6f4 v[2:5], v[138:145], v[194:201], v[238:241]
	s_setprio 0
	s_barrier
	s_add_i32 s61, s61, 2
	s_add_u32 s59, s59, 0x100
	s_addc_u32 s60, s60, 0
	s_add_u32 s22, s22, 0x100
	s_addc_u32 s23, s23, 0
	s_cmp_gt_u32 s61, 5
	s_cbranch_scc0 .LBB0_546
	s_and_b64 vcc, exec, s[10:11]
	s_cbranch_vccz .LBB0_549
	s_barrier

.LBB0_577:
	s_ashr_i32 s13, s12, 31
	s_lshl_b64 s[14:15], s[12:13], 18
	s_add_u32 s14, s29, s14
	s_addc_u32 s15, s30, s15
	s_and_b64 s[18:19], s[2:3], exec
	s_cselect_b32 s13, s15, s23
	s_cselect_b32 s54, s14, s22
	s_ashr_i32 s11, s10, 31
	s_lshl_b64 s[18:19], s[10:11], 18
	s_add_u32 s18, s27, s18
	s_addc_u32 s19, s28, s19
	s_and_b64 s[24:25], s[2:3], exec
	s_cselect_b32 s11, s19, s21
	s_cselect_b32 s55, s18, s20
	s_add_u32 s56, s20, 0x100
	s_addc_u32 s57, s21, 0
	s_add_u32 s20, s22, 0x80
	v_mov_b32_e32 v2, 0
	v_mov_b32_e32 v243, 1
	s_addc_u32 s21, s23, 0
	s_mov_b32 s58, -2
	v_mov_b32_e32 v3, v2
	v_mov_b32_e32 v66, v2
	v_mov_b32_e32 v67, v2
	v_mov_b32_e32 v68, v2
	v_mov_b32_e32 v69, v2
	v_mov_b32_e32 v70, v2
	v_mov_b32_e32 v71, v2
	v_mov_b32_e32 v72, v2
	v_mov_b32_e32 v73, v2
	v_mov_b32_e32 v74, v2
	v_mov_b32_e32 v75, v2
	v_mov_b32_e32 v76, v2
	v_mov_b32_e32 v77, v2
	v_mov_b32_e32 v82, v2
	v_mov_b32_e32 v83, v2
	v_mov_b32_e32 v84, v2
	v_mov_b32_e32 v85, v2
	v_mov_b32_e32 v90, v2
	v_mov_b32_e32 v91, v2
	v_mov_b32_e32 v92, v2
	v_mov_b32_e32 v93, v2
	v_mov_b32_e32 v98, v2
	v_mov_b32_e32 v99, v2
	v_mov_b32_e32 v100, v2
	v_mov_b32_e32 v101, v2
	v_mov_b32_e32 v106, v2
	v_mov_b32_e32 v107, v2
	v_mov_b32_e32 v108, v2
	v_mov_b32_e32 v109, v2
	v_mov_b32_e32 v114, v2
	v_mov_b32_e32 v115, v2
	v_mov_b32_e32 v116, v2
	v_mov_b32_e32 v117, v2
	v_mov_b32_e32 v78, v2
	v_mov_b32_e32 v79, v2
	v_mov_b32_e32 v80, v2
	v_mov_b32_e32 v81, v2
	v_mov_b32_e32 v86, v2
	v_mov_b32_e32 v87, v2
	v_mov_b32_e32 v88, v2
	v_mov_b32_e32 v89, v2
	v_mov_b32_e32 v94, v2
	v_mov_b32_e32 v95, v2
	v_mov_b32_e32 v96, v2
	v_mov_b32_e32 v97, v2
	v_mov_b32_e32 v102, v2
	v_mov_b32_e32 v103, v2
	v_mov_b32_e32 v104, v2
	v_mov_b32_e32 v105, v2
	v_mov_b32_e32 v110, v2
	v_mov_b32_e32 v111, v2
	v_mov_b32_e32 v112, v2
	v_mov_b32_e32 v113, v2
	v_mov_b32_e32 v118, v2
	v_mov_b32_e32 v119, v2
	v_mov_b32_e32 v120, v2
	v_mov_b32_e32 v121, v2
	v_mov_b32_e32 v122, v2
	v_mov_b32_e32 v123, v2
	v_mov_b32_e32 v124, v2
	v_mov_b32_e32 v125, v2
	v_mov_b32_e32 v126, v2
	v_mov_b32_e32 v127, v2
	v_mov_b32_e32 v128, v2
	v_mov_b32_e32 v129, v2
	s_branch .LBB0_578
.Llzf_3:
	v_mfma_f32_16x16x128_f8f6f4 v[126:129], v[138:145], v[170:177], v[126:129]
	v_mov_b32_e32 v4, 0
	v_mov_b32_e32 v5, 0
	v_mov_b32_e32 v6, 0
	v_mov_b32_e32 v7, 0
	v_mfma_f32_16x16x128_f8f6f4 v[122:125], v[146:153], v[170:177], v[122:125]
	v_mov_b32_e32 v8, 0
	v_mov_b32_e32 v9, 0
	v_mov_b32_e32 v10, 0
	v_mov_b32_e32 v11, 0
	v_mfma_f32_16x16x128_f8f6f4 v[118:121], v[138:145], v[186:193], v[118:121]
	v_mov_b32_e32 v12, 0
	v_mov_b32_e32 v13, 0
	v_mov_b32_e32 v18, 0
	v_mov_b32_e32 v19, 0
	v_mfma_f32_16x16x128_f8f6f4 v[110:113], v[146:153], v[186:193], v[110:113]
	v_mov_b32_e32 v20, 0
	v_mov_b32_e32 v21, 0
	v_mov_b32_e32 v26, 0
	v_mov_b32_e32 v27, 0
	v_mfma_f32_16x16x128_f8f6f4 v[102:105], v[138:145], v[194:201], v[102:105]
	v_mov_b32_e32 v28, 0
	v_mov_b32_e32 v29, 0
	v_mov_b32_e32 v34, 0
	v_mov_b32_e32 v35, 0
	v_mfma_f32_16x16x128_f8f6f4 v[178:181], v[146:153], v[194:201], v[94:97]
	v_mov_b32_e32 v36, 0
	v_mov_b32_e32 v37, 0
	v_mov_b32_e32 v42, 0
	v_mov_b32_e32 v43, 0
	v_mfma_f32_16x16x128_f8f6f4 v[210:213], v[138:145], v[202:209], v[86:89]
	v_mov_b32_e32 v44, 0
	v_mov_b32_e32 v45, 0
	v_mov_b32_e32 v50, 0
	v_mov_b32_e32 v51, 0
	v_mfma_f32_16x16x128_f8f6f4 v[214:217], v[146:153], v[202:209], v[78:81]
	v_mov_b32_e32 v52, 0
	v_mov_b32_e32 v53, 0
	v_mov_b32_e32 v14, 0
	v_mov_b32_e32 v15, 0
	s_setprio 0
	s_setprio 1
	v_mfma_f32_16x16x128_f8f6f4 v[114:117], v[154:161], v[170:177], v[114:117]
	v_mov_b32_e32 v16, 0
	v_mov_b32_e32 v17, 0
	v_mov_b32_e32 v22, 0
	v_mov_b32_e32 v23, 0
	v_mfma_f32_16x16x128_f8f6f4 v[106:109], v[162:169], v[170:177], v[106:109]
	v_mov_b32_e32 v24, 0
	v_mov_b32_e32 v25, 0
	v_mov_b32_e32 v30, 0
	v_mov_b32_e32 v31, 0
	v_mfma_f32_16x16x128_f8f6f4 v[98:101], v[154:161], v[186:193], v[98:101]
	v_mov_b32_e32 v32, 0
	v_mov_b32_e32 v33, 0
	v_mov_b32_e32 v38, 0
	v_mov_b32_e32 v39, 0
	v_mfma_f32_16x16x128_f8f6f4 v[170:173], v[162:169], v[186:193], v[90:93]
	v_mov_b32_e32 v40, 0
	v_mov_b32_e32 v41, 0
	v_mov_b32_e32 v46, 0
	v_mov_b32_e32 v47, 0
	v_mfma_f32_16x16x128_f8f6f4 v[174:177], v[154:161], v[194:201], v[82:85]
	v_mov_b32_e32 v48, 0
	v_mov_b32_e32 v49, 0
	v_mov_b32_e32 v54, 0
	v_mov_b32_e32 v55, 0
	v_mfma_f32_16x16x128_f8f6f4 v[186:189], v[162:169], v[194:201], v[74:77]
	v_mov_b32_e32 v56, 0
	v_mov_b32_e32 v57, 0
	v_mov_b32_e32 v58, 0
	v_mov_b32_e32 v59, 0
	v_mfma_f32_16x16x128_f8f6f4 v[190:193], v[154:161], v[202:209], v[70:73]
	v_mov_b32_e32 v60, 0
	v_mov_b32_e32 v61, 0
	v_mov_b32_e32 v62, 0
	v_mov_b32_e32 v63, 0
	v_mfma_f32_16x16x128_f8f6f4 v[194:197], v[162:169], v[202:209], v[66:69]
	v_mov_b32_e32 v64, 0
	v_mov_b32_e32 v65, 0
	s_branch .Llzj_3
.LBB0_578:
	v_add_u32_e32 v0, s17, v136
	ds_read_b128 v[138:141], v0
	ds_read_b128 v[142:145], v0 offset:1024
	ds_read_b128 v[146:149], v0 offset:2048
	ds_read_b128 v[150:153], v0 offset:3072
	v_add_u32_e32 v0, s34, v136
	ds_read_b128 v[154:157], v0
	ds_read_b128 v[158:161], v0 offset:1024
	ds_read_b128 v[162:165], v0 offset:2048
	ds_read_b128 v[166:169], v0 offset:3072
	s_add_u32 s22, s20, 0x80
	s_addc_u32 s23, s21, 0
	s_cmp_eq_u32 s58, 4
	s_cselect_b32 s23, s13, s23
	s_cselect_b32 s22, s54, s22
	s_cselect_b32 s25, s11, s57
	s_cselect_b32 s24, s55, s56
	v_mov_b32_e32 v0, v133
	ds_read_b128 v[170:173], v137
	ds_read_b128 v[174:177], v137 offset:1024
	ds_read_b128 v[186:189], v137 offset:2048
	ds_read_b128 v[190:193], v137 offset:3072
	ds_read_b128 v[194:197], v137 offset:4096
	ds_read_b128 v[198:201], v137 offset:5120
	ds_read_b128 v[202:205], v137 offset:6144
	ds_read_b128 v[206:209], v137 offset:7168
	s_add_i32 m0, s37, 0xc000
	v_add_u32_e32 v0, 0x20000, v0
	global_load_lds_dwordx4 v0, s[20:21]
	v_mov_b32_e32 v0, v135
	s_add_i32 m0, s37, 0xe000
	v_add_u32_e32 v0, 0x20000, v0
	global_load_lds_dwordx4 v0, s[20:21]
	s_waitcnt vmcnt(8)
	s_waitcnt lgkmcnt(0)
	s_barrier
	s_setprio 1
	s_waitcnt lgkmcnt(0)
	s_cmp_eq_u32 s58, -2
	s_cbranch_scc1 .Llzf_3
	v_mfma_f32_16x16x128_f8f6f4 v[126:129], v[138:145], v[170:177], v[126:129]
	v_mfma_f32_16x16x128_f8f6f4 v[122:125], v[146:153], v[170:177], v[122:125]
	v_mfma_f32_16x16x128_f8f6f4 v[118:121], v[138:145], v[186:193], v[118:121]
	v_mfma_f32_16x16x128_f8f6f4 v[110:113], v[146:153], v[186:193], v[110:113]
	v_mfma_f32_16x16x128_f8f6f4 v[102:105], v[138:145], v[194:201], v[102:105]
	v_mfma_f32_16x16x128_f8f6f4 v[178:181], v[146:153], v[194:201], v[94:97]
	v_mfma_f32_16x16x128_f8f6f4 v[210:213], v[138:145], v[202:209], v[86:89]
	v_mfma_f32_16x16x128_f8f6f4 v[214:217], v[146:153], v[202:209], v[78:81]
	s_setprio 0
	s_setprio 1
	v_mfma_f32_16x16x128_f8f6f4 v[114:117], v[154:161], v[170:177], v[114:117]
	v_mfma_f32_16x16x128_f8f6f4 v[106:109], v[162:169], v[170:177], v[106:109]
	v_mfma_f32_16x16x128_f8f6f4 v[98:101], v[154:161], v[186:193], v[98:101]
	v_mfma_f32_16x16x128_f8f6f4 v[170:173], v[162:169], v[186:193], v[90:93]
	v_mfma_f32_16x16x128_f8f6f4 v[174:177], v[154:161], v[194:201], v[82:85]
	v_mfma_f32_16x16x128_f8f6f4 v[186:189], v[162:169], v[194:201], v[74:77]
	v_mfma_f32_16x16x128_f8f6f4 v[190:193], v[154:161], v[202:209], v[70:73]
	v_mfma_f32_16x16x128_f8f6f4 v[194:197], v[162:169], v[202:209], v[66:69]
.Llzj_3:
	s_setprio 0
	s_barrier
	v_mov_b32_e32 v0, v132
	s_mov_b32 m0, s31
	s_nop 2
	ds_read_b128 v[66:69], v137 offset:16384
	ds_read_b128 v[70:73], v137 offset:17408
	ds_read_b128 v[74:77], v137 offset:18432
	ds_read_b128 v[78:81], v137 offset:19456
	ds_read_b128 v[82:85], v137 offset:20480
	ds_read_b128 v[86:89], v137 offset:21504
	ds_read_b128 v[90:93], v137 offset:22528
	ds_read_b128 v[94:97], v137 offset:23552
	s_add_u32 s60, s24, 0x20000
	global_load_lds_dwordx4 v0, s[24:25]
	v_mov_b32_e32 v0, v134
	s_mov_b32 m0, s33
	s_addc_u32 s61, s25, 0
	global_load_lds_dwordx4 v0, s[24:25]
	v_mov_b32_e32 v0, v132
	s_mov_b32 m0, s35
	s_nop 0
	global_load_lds_dwordx4 v0, s[60:61]
	v_mov_b32_e32 v0, v134
	s_mov_b32 m0, s36
	s_nop 0
	global_load_lds_dwordx4 v0, s[60:61]
	v_mov_b32_e32 v0, v133
	s_mov_b32 m0, s37
	s_nop 0
	global_load_lds_dwordx4 v0, s[22:23]
	v_mov_b32_e32 v0, v135
	s_mov_b32 m0, s38
	s_nop 0
	global_load_lds_dwordx4 v0, s[22:23]
	s_waitcnt vmcnt(8)
	s_waitcnt lgkmcnt(0)
	s_barrier
	s_setprio 1
	s_waitcnt lgkmcnt(0)
	v_mfma_f32_16x16x128_f8f6f4 v[62:65], v[138:145], v[66:73], v[62:65]
	v_mfma_f32_16x16x128_f8f6f4 v[58:61], v[146:153], v[66:73], v[58:61]
	v_mfma_f32_16x16x128_f8f6f4 v[54:57], v[138:145], v[74:81], v[54:57]
	v_mfma_f32_16x16x128_f8f6f4 v[198:201], v[146:153], v[74:81], v[46:49]
	v_mfma_f32_16x16x128_f8f6f4 v[202:205], v[138:145], v[82:89], v[38:41]
	v_mfma_f32_16x16x128_f8f6f4 v[206:209], v[146:153], v[82:89], v[30:33]
	v_mfma_f32_16x16x128_f8f6f4 v[218:221], v[138:145], v[90:97], v[22:25]
	v_mfma_f32_16x16x128_f8f6f4 v[222:225], v[146:153], v[90:97], v[14:17]
	s_setprio 0
	s_setprio 1
	v_mfma_f32_16x16x128_f8f6f4 v[50:53], v[154:161], v[66:73], v[50:53]
	v_mfma_f32_16x16x128_f8f6f4 v[226:229], v[162:169], v[66:73], v[42:45]
	v_mfma_f32_16x16x128_f8f6f4 v[230:233], v[154:161], v[74:81], v[34:37]
	v_mfma_f32_16x16x128_f8f6f4 v[234:237], v[162:169], v[74:81], v[26:29]
	v_mfma_f32_16x16x128_f8f6f4 v[238:241], v[154:161], v[82:89], v[18:21]
	v_mfma_f32_16x16x128_f8f6f4 v[244:247], v[162:169], v[82:89], v[10:13]
	v_mfma_f32_16x16x128_f8f6f4 v[248:251], v[154:161], v[90:97], v[6:9]
	v_mfma_f32_16x16x128_f8f6f4 v[182:185], v[162:169], v[90:97], v[2:5]
	s_setprio 0
	s_barrier
	v_add_u32_e32 v0, s43, v136
	s_nop 3
	ds_read_b128 v[2:5], v0
	ds_read_b128 v[6:9], v0 offset:1024
	ds_read_b128 v[10:13], v0 offset:2048
	ds_read_b128 v[14:17], v0 offset:3072
	v_add_u32_e32 v0, s48, v136
	ds_read_b128 v[138:141], v0
	ds_read_b128 v[142:145], v0 offset:1024
	ds_read_b128 v[146:149], v0 offset:2048
	ds_read_b128 v[150:153], v0 offset:3072
	v_mov_b32_e32 v0, v133
	ds_read_b128 v[18:21], v137 offset:32768
	ds_read_b128 v[22:25], v137 offset:33792
	ds_read_b128 v[26:29], v137 offset:34816
	ds_read_b128 v[30:33], v137 offset:35840
	ds_read_b128 v[34:37], v137 offset:36864
	ds_read_b128 v[38:41], v137 offset:37888
	ds_read_b128 v[42:45], v137 offset:38912
	ds_read_b128 v[46:49], v137 offset:39936
	s_mov_b32 m0, s39
	v_add_u32_e32 v0, 0x20000, v0
	global_load_lds_dwordx4 v0, s[22:23]
	v_mov_b32_e32 v0, v135
	s_mov_b32 m0, s40
	v_add_u32_e32 v0, 0x20000, v0
	global_load_lds_dwordx4 v0, s[22:23]
	s_waitcnt vmcnt(8)
	s_waitcnt lgkmcnt(0)
	s_barrier
	s_setprio 1
	s_waitcnt lgkmcnt(0)
	v_mfma_f32_16x16x128_f8f6f4 v[126:129], v[2:9], v[18:25], v[126:129]
	v_mfma_f32_16x16x128_f8f6f4 v[122:125], v[10:17], v[18:25], v[122:125]
	v_mfma_f32_16x16x128_f8f6f4 v[118:121], v[2:9], v[26:33], v[118:121]
	v_mfma_f32_16x16x128_f8f6f4 v[110:113], v[10:17], v[26:33], v[110:113]
	v_mfma_f32_16x16x128_f8f6f4 v[102:105], v[2:9], v[34:41], v[102:105]
	v_mfma_f32_16x16x128_f8f6f4 v[94:97], v[10:17], v[34:41], v[178:181]
	v_mfma_f32_16x16x128_f8f6f4 v[86:89], v[2:9], v[42:49], v[210:213]
	v_mfma_f32_16x16x128_f8f6f4 v[78:81], v[10:17], v[42:49], v[214:217]
	s_setprio 0
	s_setprio 1
	v_mfma_f32_16x16x128_f8f6f4 v[114:117], v[138:145], v[18:25], v[114:117]
	v_mfma_f32_16x16x128_f8f6f4 v[106:109], v[146:153], v[18:25], v[106:109]
	v_mfma_f32_16x16x128_f8f6f4 v[98:101], v[138:145], v[26:33], v[98:101]
	v_mfma_f32_16x16x128_f8f6f4 v[90:93], v[146:153], v[26:33], v[170:173]
	v_mfma_f32_16x16x128_f8f6f4 v[82:85], v[138:145], v[34:41], v[174:177]
	v_mfma_f32_16x16x128_f8f6f4 v[74:77], v[146:153], v[34:41], v[186:189]
	v_mfma_f32_16x16x128_f8f6f4 v[70:73], v[138:145], v[42:49], v[190:193]
	v_mfma_f32_16x16x128_f8f6f4 v[66:69], v[146:153], v[42:49], v[194:197]
	s_setprio 0
	s_barrier
	v_mov_b32_e32 v0, v132
	ds_read_b128 v[154:157], v137 offset:49152
	ds_read_b128 v[158:161], v137 offset:50176
	ds_read_b128 v[162:165], v137 offset:51200
	ds_read_b128 v[166:169], v137 offset:52224
	ds_read_b128 v[170:173], v137 offset:53248
	ds_read_b128 v[174:177], v137 offset:54272
	ds_read_b128 v[186:189], v137 offset:55296
	ds_read_b128 v[190:193], v137 offset:56320
	s_mov_b32 m0, s44
	v_lshl_add_u64 v[18:19], s[24:25], 0, v[0:1]
	v_lshl_add_u64 v[18:19], v[18:19], 0, s[82:83]
	v_mov_b32_e32 v0, v134
	global_load_lds_dwordx4 v[18:19], off
	s_mov_b32 m0, s45
	v_lshl_add_u64 v[18:19], s[24:25], 0, v[0:1]
	v_lshl_add_u64 v[18:19], v[18:19], 0, s[82:83]
	s_add_u32 s24, s24, 0x20080
	v_mov_b32_e32 v0, v132
	global_load_lds_dwordx4 v[18:19], off
	s_addc_u32 s25, s25, 0
	s_mov_b32 m0, s49
	s_nop 0
	global_load_lds_dwordx4 v0, s[24:25]
	v_mov_b32_e32 v0, v134
	s_mov_b32 m0, s50
	s_nop 0
	global_load_lds_dwordx4 v0, s[24:25]
	v_mov_b32_e32 v0, v133
	s_mov_b32 m0, s46
	v_lshl_add_u64 v[18:19], s[22:23], 0, v[0:1]
	v_lshl_add_u64 v[18:19], v[18:19], 0, s[82:83]
	v_mov_b32_e32 v0, v135
	global_load_lds_dwordx4 v[18:19], off
	s_mov_b32 m0, s47
	v_lshl_add_u64 v[18:19], s[22:23], 0, v[0:1]
	v_lshl_add_u64 v[18:19], v[18:19], 0, s[82:83]
	global_load_lds_dwordx4 v[18:19], off
	s_waitcnt vmcnt(8)
	s_waitcnt lgkmcnt(0)
	s_barrier
	s_setprio 1
	s_waitcnt lgkmcnt(0)
	v_mfma_f32_16x16x128_f8f6f4 v[62:65], v[2:9], v[154:161], v[62:65]
	v_mfma_f32_16x16x128_f8f6f4 v[58:61], v[10:17], v[154:161], v[58:61]
	v_mfma_f32_16x16x128_f8f6f4 v[54:57], v[2:9], v[162:169], v[54:57]
	v_mfma_f32_16x16x128_f8f6f4 v[46:49], v[10:17], v[162:169], v[198:201]
	v_mfma_f32_16x16x128_f8f6f4 v[38:41], v[2:9], v[170:177], v[202:205]
	v_mfma_f32_16x16x128_f8f6f4 v[30:33], v[10:17], v[170:177], v[206:209]
	v_mfma_f32_16x16x128_f8f6f4 v[22:25], v[2:9], v[186:193], v[218:221]
	v_mfma_f32_16x16x128_f8f6f4 v[14:17], v[10:17], v[186:193], v[222:225]
	s_setprio 0
	s_setprio 1
	v_mfma_f32_16x16x128_f8f6f4 v[50:53], v[138:145], v[154:161], v[50:53]
	v_mfma_f32_16x16x128_f8f6f4 v[42:45], v[146:153], v[154:161], v[226:229]
	v_mfma_f32_16x16x128_f8f6f4 v[34:37], v[138:145], v[162:169], v[230:233]
	v_mfma_f32_16x16x128_f8f6f4 v[26:29], v[146:153], v[162:169], v[234:237]
	v_mfma_f32_16x16x128_f8f6f4 v[18:21], v[138:145], v[170:177], v[238:241]
	v_mfma_f32_16x16x128_f8f6f4 v[10:13], v[146:153], v[170:177], v[244:247]
	v_mfma_f32_16x16x128_f8f6f4 v[6:9], v[138:145], v[186:193], v[248:251]
	v_mfma_f32_16x16x128_f8f6f4 v[2:5], v[146:153], v[186:193], v[182:185]
	s_setprio 0
	s_barrier
	s_add_i32 s58, s58, 2
	s_add_u32 s56, s56, 0x100
	s_addc_u32 s57, s57, 0
	s_add_u32 s20, s20, 0x100
	s_addc_u32 s21, s21, 0
	s_cmp_gt_u32 s58, 5
	s_cbranch_scc0 .LBB0_578
	s_and_b64 vcc, exec, s[8:9]
	s_cbranch_vccz .LBB0_581
	s_barrier

.Llzf_4:
	v_mfma_f32_16x16x128_f8f6f4 v[126:129], v[130:137], v[186:193], v[126:129]
	v_mov_b32_e32 v4, 0
	v_mov_b32_e32 v5, 0
	v_mov_b32_e32 v6, 0
	v_mov_b32_e32 v7, 0
	v_mfma_f32_16x16x128_f8f6f4 v[122:125], v[138:145], v[186:193], v[122:125]
	v_mov_b32_e32 v8, 0
	v_mov_b32_e32 v9, 0
	v_mov_b32_e32 v14, 0
	v_mov_b32_e32 v15, 0
	v_mfma_f32_16x16x128_f8f6f4 v[110:113], v[130:137], v[194:201], v[110:113]
	v_mov_b32_e32 v16, 0
	v_mov_b32_e32 v17, 0
	v_mov_b32_e32 v22, 0
	v_mov_b32_e32 v23, 0
	v_mfma_f32_16x16x128_f8f6f4 v[106:109], v[138:145], v[194:201], v[106:109]
	v_mov_b32_e32 v24, 0
	v_mov_b32_e32 v25, 0
	v_mov_b32_e32 v30, 0
	v_mov_b32_e32 v31, 0
	v_mfma_f32_16x16x128_f8f6f4 v[98:101], v[130:137], v[202:209], v[98:101]
	v_mov_b32_e32 v32, 0
	v_mov_b32_e32 v33, 0
	v_mov_b32_e32 v38, 0
	v_mov_b32_e32 v39, 0
	v_mfma_f32_16x16x128_f8f6f4 v[162:165], v[138:145], v[202:209], v[90:93]
	v_mov_b32_e32 v40, 0
	v_mov_b32_e32 v41, 0
	v_mov_b32_e32 v46, 0
	v_mov_b32_e32 v47, 0
	v_mfma_f32_16x16x128_f8f6f4 v[172:175], v[130:137], v[210:217], v[82:85]
	v_mov_b32_e32 v48, 0
	v_mov_b32_e32 v49, 0
	v_mov_b32_e32 v54, 0
	v_mov_b32_e32 v55, 0
	v_mfma_f32_16x16x128_f8f6f4 v[176:179], v[138:145], v[210:217], v[74:77]
	v_mov_b32_e32 v56, 0
	v_mov_b32_e32 v57, 0
	v_mov_b32_e32 v10, 0
	v_mov_b32_e32 v11, 0
	s_setprio 0
	s_setprio 1
	v_mfma_f32_16x16x128_f8f6f4 v[118:121], v[146:153], v[186:193], v[118:121]
	v_mov_b32_e32 v12, 0
	v_mov_b32_e32 v13, 0
	v_mov_b32_e32 v18, 0
	v_mov_b32_e32 v19, 0
	v_mfma_f32_16x16x128_f8f6f4 v[114:117], v[154:161], v[186:193], v[114:117]
	v_mov_b32_e32 v20, 0
	v_mov_b32_e32 v21, 0
	v_mov_b32_e32 v26, 0
	v_mov_b32_e32 v27, 0
	v_mfma_f32_16x16x128_f8f6f4 v[102:105], v[146:153], v[194:201], v[102:105]
	v_mov_b32_e32 v28, 0
	v_mov_b32_e32 v29, 0
	v_mov_b32_e32 v34, 0
	v_mov_b32_e32 v35, 0
	v_mfma_f32_16x16x128_f8f6f4 v[180:183], v[154:161], v[194:201], v[94:97]
	v_mov_b32_e32 v36, 0
	v_mov_b32_e32 v37, 0
	v_mov_b32_e32 v42, 0
	v_mov_b32_e32 v43, 0
	v_mfma_f32_16x16x128_f8f6f4 v[184:187], v[146:153], v[202:209], v[86:89]
	v_mov_b32_e32 v44, 0
	v_mov_b32_e32 v45, 0
	v_mov_b32_e32 v50, 0
	v_mov_b32_e32 v51, 0
	v_mfma_f32_16x16x128_f8f6f4 v[188:191], v[154:161], v[202:209], v[78:81]
	v_mov_b32_e32 v52, 0
	v_mov_b32_e32 v53, 0
	v_mov_b32_e32 v58, 0
	v_mov_b32_e32 v59, 0
	v_mfma_f32_16x16x128_f8f6f4 v[192:195], v[146:153], v[210:217], v[70:73]
	v_mov_b32_e32 v60, 0
	v_mov_b32_e32 v61, 0
	v_mov_b32_e32 v62, 0
	v_mov_b32_e32 v63, 0
	v_mfma_f32_16x16x128_f8f6f4 v[196:199], v[154:161], v[210:217], v[66:69]
	v_mov_b32_e32 v64, 0
	v_mov_b32_e32 v65, 0
	s_branch .Llzj_4
.LBB0_595:
	v_add_u32_e32 v0, s21, v170
	ds_read_b128 v[130:133], v0
	ds_read_b128 v[134:137], v0 offset:1024
	ds_read_b128 v[138:141], v0 offset:2048
	ds_read_b128 v[142:145], v0 offset:3072
	v_add_u32_e32 v0, s39, v170
	ds_read_b128 v[146:149], v0
	ds_read_b128 v[150:153], v0 offset:1024
	ds_read_b128 v[154:157], v0 offset:2048
	ds_read_b128 v[158:161], v0 offset:3072
	s_add_u32 s24, s22, 0x80
	s_addc_u32 s25, s23, 0
	s_cmp_eq_u32 s61, 4
	s_cselect_b32 s25, s1, s25
	s_cselect_b32 s24, s15, s24
	s_cselect_b32 s27, s13, s60
	s_cselect_b32 s26, s33, s59
	v_mov_b32_e32 v0, v167
	ds_read_b128 v[186:189], v171
	ds_read_b128 v[190:193], v171 offset:1024
	ds_read_b128 v[194:197], v171 offset:2048
	ds_read_b128 v[198:201], v171 offset:3072
	ds_read_b128 v[202:205], v171 offset:4096
	ds_read_b128 v[206:209], v171 offset:5120
	ds_read_b128 v[210:213], v171 offset:6144
	ds_read_b128 v[214:217], v171 offset:7168
	s_add_i32 m0, s42, 0xc000
	v_add_u32_e32 v0, 0x20000, v0
	global_load_lds_dwordx4 v0, s[22:23]
	v_mov_b32_e32 v0, v169
	s_add_i32 m0, s42, 0xe000
	v_add_u32_e32 v0, 0x20000, v0
	global_load_lds_dwordx4 v0, s[22:23]
	s_waitcnt vmcnt(8)
	s_waitcnt lgkmcnt(0)
	s_barrier
	s_setprio 1
	s_waitcnt lgkmcnt(0)
	s_cmp_eq_u32 s61, -2
	s_cbranch_scc1 .Llzf_4
	v_mfma_f32_16x16x128_f8f6f4 v[126:129], v[130:137], v[186:193], v[126:129]
	v_mfma_f32_16x16x128_f8f6f4 v[122:125], v[138:145], v[186:193], v[122:125]
	v_mfma_f32_16x16x128_f8f6f4 v[110:113], v[130:137], v[194:201], v[110:113]
	v_mfma_f32_16x16x128_f8f6f4 v[106:109], v[138:145], v[194:201], v[106:109]
	v_mfma_f32_16x16x128_f8f6f4 v[98:101], v[130:137], v[202:209], v[98:101]
	v_mfma_f32_16x16x128_f8f6f4 v[162:165], v[138:145], v[202:209], v[90:93]
	v_mfma_f32_16x16x128_f8f6f4 v[172:175], v[130:137], v[210:217], v[82:85]
	v_mfma_f32_16x16x128_f8f6f4 v[176:179], v[138:145], v[210:217], v[74:77]
	s_setprio 0
	s_setprio 1
	v_mfma_f32_16x16x128_f8f6f4 v[118:121], v[146:153], v[186:193], v[118:121]
	v_mfma_f32_16x16x128_f8f6f4 v[114:117], v[154:161], v[186:193], v[114:117]
	v_mfma_f32_16x16x128_f8f6f4 v[102:105], v[146:153], v[194:201], v[102:105]
	v_mfma_f32_16x16x128_f8f6f4 v[180:183], v[154:161], v[194:201], v[94:97]
	v_mfma_f32_16x16x128_f8f6f4 v[184:187], v[146:153], v[202:209], v[86:89]
	v_mfma_f32_16x16x128_f8f6f4 v[188:191], v[154:161], v[202:209], v[78:81]
	v_mfma_f32_16x16x128_f8f6f4 v[192:195], v[146:153], v[210:217], v[70:73]
	v_mfma_f32_16x16x128_f8f6f4 v[196:199], v[154:161], v[210:217], v[66:69]
.Llzj_4:
	s_setprio 0
	s_barrier
	v_mov_b32_e32 v0, v166
	s_mov_b32 m0, s37
	s_nop 2
	ds_read_b128 v[66:69], v171 offset:16384
	ds_read_b128 v[70:73], v171 offset:17408
	ds_read_b128 v[74:77], v171 offset:18432
	ds_read_b128 v[78:81], v171 offset:19456
	ds_read_b128 v[82:85], v171 offset:20480
	ds_read_b128 v[86:89], v171 offset:21504
	ds_read_b128 v[90:93], v171 offset:22528
	ds_read_b128 v[94:97], v171 offset:23552
	s_add_u32 s62, s26, 0x20000
	global_load_lds_dwordx4 v0, s[26:27]
	v_mov_b32_e32 v0, v168
	s_mov_b32 m0, s38
	s_addc_u32 s63, s27, 0
	global_load_lds_dwordx4 v0, s[26:27]
	v_mov_b32_e32 v0, v166
	s_mov_b32 m0, s40
	s_nop 0
	global_load_lds_dwordx4 v0, s[62:63]
	v_mov_b32_e32 v0, v168
	s_mov_b32 m0, s41
	s_nop 0
	global_load_lds_dwordx4 v0, s[62:63]
	v_mov_b32_e32 v0, v167
	s_mov_b32 m0, s42
	s_nop 0
	global_load_lds_dwordx4 v0, s[24:25]
	v_mov_b32_e32 v0, v169
	s_mov_b32 m0, s43
	s_nop 0
	global_load_lds_dwordx4 v0, s[24:25]
	s_waitcnt vmcnt(8)
	s_waitcnt lgkmcnt(0)
	s_barrier
	s_setprio 1
	s_waitcnt lgkmcnt(0)
	v_mfma_f32_16x16x128_f8f6f4 v[62:65], v[130:137], v[66:73], v[62:65]
	v_mfma_f32_16x16x128_f8f6f4 v[58:61], v[138:145], v[66:73], v[58:61]
	v_mfma_f32_16x16x128_f8f6f4 v[50:53], v[130:137], v[74:81], v[50:53]
	v_mfma_f32_16x16x128_f8f6f4 v[202:205], v[138:145], v[74:81], v[42:45]
	v_mfma_f32_16x16x128_f8f6f4 v[206:209], v[130:137], v[82:89], v[34:37]
	v_mfma_f32_16x16x128_f8f6f4 v[210:213], v[138:145], v[82:89], v[26:29]
	v_mfma_f32_16x16x128_f8f6f4 v[214:217], v[130:137], v[90:97], v[18:21]
	v_mfma_f32_16x16x128_f8f6f4 v[218:221], v[138:145], v[90:97], v[10:13]
	s_setprio 0
	s_setprio 1
	v_mfma_f32_16x16x128_f8f6f4 v[54:57], v[146:153], v[66:73], v[54:57]
	v_mfma_f32_16x16x128_f8f6f4 v[222:225], v[154:161], v[66:73], v[46:49]
	v_mfma_f32_16x16x128_f8f6f4 v[226:229], v[146:153], v[74:81], v[38:41]
	v_mfma_f32_16x16x128_f8f6f4 v[230:233], v[154:161], v[74:81], v[30:33]
	v_mfma_f32_16x16x128_f8f6f4 v[234:237], v[146:153], v[82:89], v[22:25]
	v_mfma_f32_16x16x128_f8f6f4 v[238:241], v[154:161], v[82:89], v[14:17]
	v_mfma_f32_16x16x128_f8f6f4 v[244:247], v[146:153], v[90:97], v[6:9]
	v_mfma_f32_16x16x128_f8f6f4 v[248:251], v[154:161], v[90:97], v[2:5]
	s_setprio 0
	s_barrier
	v_add_u32_e32 v0, s48, v170
	s_nop 3
	ds_read_b128 v[2:5], v0
	ds_read_b128 v[6:9], v0 offset:1024
	ds_read_b128 v[10:13], v0 offset:2048
	ds_read_b128 v[14:17], v0 offset:3072
	v_add_u32_e32 v0, s53, v170
	ds_read_b128 v[130:133], v0
	ds_read_b128 v[134:137], v0 offset:1024
	ds_read_b128 v[138:141], v0 offset:2048
	ds_read_b128 v[142:145], v0 offset:3072
	v_mov_b32_e32 v0, v167
	ds_read_b128 v[18:21], v171 offset:32768
	ds_read_b128 v[22:25], v171 offset:33792
	ds_read_b128 v[26:29], v171 offset:34816
	ds_read_b128 v[30:33], v171 offset:35840
	ds_read_b128 v[34:37], v171 offset:36864
	ds_read_b128 v[38:41], v171 offset:37888
	ds_read_b128 v[42:45], v171 offset:38912
	ds_read_b128 v[46:49], v171 offset:39936
	s_mov_b32 m0, s44
	v_add_u32_e32 v0, 0x20000, v0
	global_load_lds_dwordx4 v0, s[24:25]
	v_mov_b32_e32 v0, v169
	s_mov_b32 m0, s45
	v_add_u32_e32 v0, 0x20000, v0
	global_load_lds_dwordx4 v0, s[24:25]
	s_waitcnt vmcnt(8)
	s_waitcnt lgkmcnt(0)
	s_barrier
	s_setprio 1
	s_waitcnt lgkmcnt(0)
	v_mfma_f32_16x16x128_f8f6f4 v[126:129], v[2:9], v[18:25], v[126:129]
	v_mfma_f32_16x16x128_f8f6f4 v[122:125], v[10:17], v[18:25], v[122:125]
	v_mfma_f32_16x16x128_f8f6f4 v[110:113], v[2:9], v[26:33], v[110:113]
	v_mfma_f32_16x16x128_f8f6f4 v[106:109], v[10:17], v[26:33], v[106:109]
	v_mfma_f32_16x16x128_f8f6f4 v[98:101], v[2:9], v[34:41], v[98:101]
	v_mfma_f32_16x16x128_f8f6f4 v[90:93], v[10:17], v[34:41], v[162:165]
	v_mfma_f32_16x16x128_f8f6f4 v[82:85], v[2:9], v[42:49], v[172:175]
	v_mfma_f32_16x16x128_f8f6f4 v[74:77], v[10:17], v[42:49], v[176:179]
	s_setprio 0
	s_setprio 1
	v_mfma_f32_16x16x128_f8f6f4 v[118:121], v[130:137], v[18:25], v[118:121]
	v_mfma_f32_16x16x128_f8f6f4 v[114:117], v[138:145], v[18:25], v[114:117]
	v_mfma_f32_16x16x128_f8f6f4 v[102:105], v[130:137], v[26:33], v[102:105]
	v_mfma_f32_16x16x128_f8f6f4 v[94:97], v[138:145], v[26:33], v[180:183]
	v_mfma_f32_16x16x128_f8f6f4 v[86:89], v[130:137], v[34:41], v[184:187]
	v_mfma_f32_16x16x128_f8f6f4 v[78:81], v[138:145], v[34:41], v[188:191]
	v_mfma_f32_16x16x128_f8f6f4 v[70:73], v[130:137], v[42:49], v[192:195]
	v_mfma_f32_16x16x128_f8f6f4 v[66:69], v[138:145], v[42:49], v[196:199]
	s_setprio 0
	s_barrier
	v_mov_b32_e32 v0, v166
	ds_read_b128 v[146:149], v171 offset:49152
	ds_read_b128 v[150:153], v171 offset:50176
	ds_read_b128 v[154:157], v171 offset:51200
	ds_read_b128 v[158:161], v171 offset:52224
	ds_read_b128 v[186:189], v171 offset:53248
	ds_read_b128 v[190:193], v171 offset:54272
	ds_read_b128 v[194:197], v171 offset:55296
	ds_read_b128 v[198:201], v171 offset:56320
	s_mov_b32 m0, s49
	v_lshl_add_u64 v[18:19], s[26:27], 0, v[0:1]
	v_lshl_add_u64 v[18:19], v[18:19], 0, s[82:83]
	v_mov_b32_e32 v0, v168
	global_load_lds_dwordx4 v[18:19], off
	s_mov_b32 m0, s50
	v_lshl_add_u64 v[18:19], s[26:27], 0, v[0:1]
	v_lshl_add_u64 v[18:19], v[18:19], 0, s[82:83]
	s_add_u32 s26, s26, 0x20080
	v_mov_b32_e32 v0, v166
	global_load_lds_dwordx4 v[18:19], off
	s_addc_u32 s27, s27, 0
	s_mov_b32 m0, s54
	s_nop 0
	global_load_lds_dwordx4 v0, s[26:27]
	v_mov_b32_e32 v0, v168
	s_mov_b32 m0, s55
	s_nop 0
	global_load_lds_dwordx4 v0, s[26:27]
	v_mov_b32_e32 v0, v167
	s_mov_b32 m0, s51
	v_lshl_add_u64 v[18:19], s[24:25], 0, v[0:1]
	v_lshl_add_u64 v[18:19], v[18:19], 0, s[82:83]
	v_mov_b32_e32 v0, v169
	global_load_lds_dwordx4 v[18:19], off
	s_mov_b32 m0, s52
	v_lshl_add_u64 v[18:19], s[24:25], 0, v[0:1]
	v_lshl_add_u64 v[18:19], v[18:19], 0, s[82:83]
	global_load_lds_dwordx4 v[18:19], off
	s_waitcnt vmcnt(8)
	s_waitcnt lgkmcnt(0)
	s_barrier
	s_setprio 1
	s_waitcnt lgkmcnt(0)
	v_mfma_f32_16x16x128_f8f6f4 v[62:65], v[2:9], v[146:153], v[62:65]
	v_mfma_f32_16x16x128_f8f6f4 v[58:61], v[10:17], v[146:153], v[58:61]
	v_mfma_f32_16x16x128_f8f6f4 v[50:53], v[2:9], v[154:161], v[50:53]
	v_mfma_f32_16x16x128_f8f6f4 v[42:45], v[10:17], v[154:161], v[202:205]
	v_mfma_f32_16x16x128_f8f6f4 v[34:37], v[2:9], v[186:193], v[206:209]
	v_mfma_f32_16x16x128_f8f6f4 v[26:29], v[10:17], v[186:193], v[210:213]
	v_mfma_f32_16x16x128_f8f6f4 v[18:21], v[2:9], v[194:201], v[214:217]
	v_mfma_f32_16x16x128_f8f6f4 v[10:13], v[10:17], v[194:201], v[218:221]
	s_setprio 0
	s_setprio 1
	v_mfma_f32_16x16x128_f8f6f4 v[54:57], v[130:137], v[146:153], v[54:57]
	v_mfma_f32_16x16x128_f8f6f4 v[46:49], v[138:145], v[146:153], v[222:225]
	v_mfma_f32_16x16x128_f8f6f4 v[38:41], v[130:137], v[154:161], v[226:229]
	v_mfma_f32_16x16x128_f8f6f4 v[30:33], v[138:145], v[154:161], v[230:233]
	v_mfma_f32_16x16x128_f8f6f4 v[22:25], v[130:137], v[186:193], v[234:237]
	v_mfma_f32_16x16x128_f8f6f4 v[14:17], v[138:145], v[186:193], v[238:241]
	v_mfma_f32_16x16x128_f8f6f4 v[6:9], v[130:137], v[194:201], v[244:247]
	v_mfma_f32_16x16x128_f8f6f4 v[2:5], v[138:145], v[194:201], v[248:251]
	s_setprio 0
	s_barrier
	s_add_i32 s61, s61, 2
	s_add_u32 s59, s59, 0x100
	s_addc_u32 s60, s60, 0
	s_add_u32 s22, s22, 0x100
	s_addc_u32 s23, s23, 0
	s_cmp_gt_u32 s61, 5
	s_cbranch_scc0 .LBB0_595
	s_and_b64 vcc, exec, s[10:11]
	s_cbranch_vccz .LBB0_598
	s_barrier

.LBB0_1242:
	s_ashr_i32 s23, s22, 31
	s_lshl_b64 s[24:25], s[22:23], 21
	s_add_u32 s23, s1, s24
	s_addc_u32 s30, s33, s25
	s_ashr_i32 s21, s20, 31
	s_lshl_b64 s[24:25], s[20:21], 18
	s_add_u32 s24, s23, s24
	s_addc_u32 s25, s30, s25
	s_and_b64 s[30:31], s[2:3], exec
	s_cselect_b32 s21, s25, s29
	s_cselect_b32 s23, s24, s28
	s_lshl_b32 s64, s63, 10
	s_add_u32 s65, s28, 0x100
	v_mov_b32_e32 v2, 0
	s_addc_u32 s66, s29, 0
	s_mov_b32 s67, -2
	s_mov_b64 s[28:29], s[12:13]
	v_mov_b32_e32 v3, v2
	v_mov_b64_e32 v[70:71], v[2:3]
	v_mov_b64_e32 v[72:73], v[2:3]
	v_mov_b64_e32 v[86:87], v[2:3]
	v_mov_b64_e32 v[88:89], v[2:3]
	v_mov_b64_e32 v[98:99], v[2:3]
	s_waitcnt vmcnt(0)
	v_mov_b64_e32 v[100:101], v[2:3]
	v_mov_b64_e32 v[106:107], v[2:3]
	v_mov_b64_e32 v[108:109], v[2:3]
	v_mov_b64_e32 v[114:115], v[2:3]
	v_mov_b64_e32 v[116:117], v[2:3]
	v_mov_b64_e32 v[122:123], v[2:3]
	v_mov_b64_e32 v[124:125], v[2:3]
	v_mov_b64_e32 v[130:131], v[2:3]
	v_mov_b64_e32 v[132:133], v[2:3]
	v_mov_b64_e32 v[138:139], v[2:3]
	v_mov_b64_e32 v[140:141], v[2:3]
	v_mov_b64_e32 v[78:79], v[2:3]
	v_mov_b64_e32 v[80:81], v[2:3]
	v_mov_b64_e32 v[94:95], v[2:3]
	v_mov_b64_e32 v[96:97], v[2:3]
	v_mov_b64_e32 v[102:103], v[2:3]
	v_mov_b64_e32 v[104:105], v[2:3]
	v_mov_b64_e32 v[110:111], v[2:3]
	v_mov_b64_e32 v[112:113], v[2:3]
	v_mov_b64_e32 v[118:119], v[2:3]
	v_mov_b64_e32 v[120:121], v[2:3]
	v_mov_b64_e32 v[126:127], v[2:3]
	v_mov_b64_e32 v[128:129], v[2:3]
	v_mov_b64_e32 v[134:135], v[2:3]
	v_mov_b64_e32 v[136:137], v[2:3]
	v_mov_b64_e32 v[142:143], v[2:3]
	v_mov_b64_e32 v[144:145], v[2:3]
	s_xor_b32 s85, s85, 0x400
	s_cmp_eq_u32 s70, 0
	s_cbranch_scc0 .Lgb_skip
	s_load_dwordx2 s[98:99], s[96:97], 0xc0
	v_mbcnt_lo_u32_b32 v248, -1, 0
	v_mbcnt_hi_u32_b32 v248, -1, v248
	v_lshlrev_b32_e32 v248, 4, v248
	v_lshl_add_u32 v249, v66, 13, v248
	s_lshl_b32 s92, s26, 10
	v_add_u32_e32 v249, s92, v249
	s_add_i32 m0, s85, 0x26800
	s_waitcnt lgkmcnt(0)
	s_add_u32 s98, s98, s18
	s_addc_u32 s99, s99, s19
	s_nop 0
	global_load_lds_dwordx4 v249, s[98:99]

.Llzf_1:
	v_mfma_f32_16x16x128_f8f6f4 v[142:145], v[154:161], v[194:201], v[142:145]
	v_mov_b32_e32 v4, 0
	v_mov_b32_e32 v5, 0
	v_mov_b32_e32 v10, 0
	v_mov_b32_e32 v11, 0
	v_mfma_f32_16x16x128_f8f6f4 v[134:137], v[162:169], v[194:201], v[134:137]
	v_mov_b32_e32 v12, 0
	v_mov_b32_e32 v13, 0
	v_mov_b32_e32 v18, 0
	v_mov_b32_e32 v19, 0
	v_mfma_f32_16x16x128_f8f6f4 v[126:129], v[154:161], v[202:209], v[126:129]
	v_mov_b32_e32 v20, 0
	v_mov_b32_e32 v21, 0
	v_mov_b32_e32 v26, 0
	v_mov_b32_e32 v27, 0
	v_mfma_f32_16x16x128_f8f6f4 v[118:121], v[162:169], v[202:209], v[118:121]
	v_mov_b32_e32 v28, 0
	v_mov_b32_e32 v29, 0
	v_mov_b32_e32 v34, 0
	v_mov_b32_e32 v35, 0
	v_mfma_f32_16x16x128_f8f6f4 v[110:113], v[154:161], v[210:217], v[110:113]
	v_mov_b32_e32 v36, 0
	v_mov_b32_e32 v37, 0
	v_mov_b32_e32 v42, 0
	v_mov_b32_e32 v43, 0
	v_mfma_f32_16x16x128_f8f6f4 v[102:105], v[162:169], v[210:217], v[102:105]
	v_mov_b32_e32 v44, 0
	v_mov_b32_e32 v45, 0
	v_mov_b32_e32 v50, 0
	v_mov_b32_e32 v51, 0
	v_mfma_f32_16x16x128_f8f6f4 v[178:181], v[154:161], v[244:251], v[94:97]
	v_mov_b32_e32 v52, 0
	v_mov_b32_e32 v53, 0
	v_mov_b32_e32 v58, 0
	v_mov_b32_e32 v59, 0
	v_mfma_f32_16x16x128_f8f6f4 v[182:185], v[162:169], v[244:251], v[78:81]
	v_mov_b32_e32 v60, 0
	v_mov_b32_e32 v61, 0
	v_mov_b32_e32 v6, 0
	v_mov_b32_e32 v7, 0
	s_setprio 0
	s_setprio 1
	v_mfma_f32_16x16x128_f8f6f4 v[138:141], v[170:177], v[194:201], v[138:141]
	v_mov_b32_e32 v8, 0
	v_mov_b32_e32 v9, 0
	v_mov_b32_e32 v14, 0
	v_mov_b32_e32 v15, 0
	v_mfma_f32_16x16x128_f8f6f4 v[130:133], v[186:193], v[194:201], v[130:133]
	v_mov_b32_e32 v16, 0
	v_mov_b32_e32 v17, 0
	v_mov_b32_e32 v22, 0
	v_mov_b32_e32 v23, 0
	v_mfma_f32_16x16x128_f8f6f4 v[122:125], v[170:177], v[202:209], v[122:125]
	v_mov_b32_e32 v24, 0
	v_mov_b32_e32 v25, 0
	v_mov_b32_e32 v30, 0
	v_mov_b32_e32 v31, 0
	v_mfma_f32_16x16x128_f8f6f4 v[114:117], v[186:193], v[202:209], v[114:117]
	v_mov_b32_e32 v32, 0
	v_mov_b32_e32 v33, 0
	v_mov_b32_e32 v38, 0
	v_mov_b32_e32 v39, 0
	v_mfma_f32_16x16x128_f8f6f4 v[106:109], v[170:177], v[210:217], v[106:109]
	v_mov_b32_e32 v40, 0
	v_mov_b32_e32 v41, 0
	v_mov_b32_e32 v46, 0
	v_mov_b32_e32 v47, 0
	v_mfma_f32_16x16x128_f8f6f4 v[194:197], v[186:193], v[210:217], v[98:101]
	v_mov_b32_e32 v48, 0
	v_mov_b32_e32 v49, 0
	v_mov_b32_e32 v54, 0
	v_mov_b32_e32 v55, 0
	v_mfma_f32_16x16x128_f8f6f4 v[198:201], v[170:177], v[244:251], v[86:89]
	v_mov_b32_e32 v56, 0
	v_mov_b32_e32 v57, 0
	v_mov_b32_e32 v62, 0
	v_mov_b32_e32 v63, 0
	v_mfma_f32_16x16x128_f8f6f4 v[202:205], v[186:193], v[244:251], v[70:73]
	v_mov_b32_e32 v64, 0
	v_mov_b32_e32 v65, 0
	s_branch .Llzj_1
.LBB0_1243:
	v_add_u32_e32 v0, s64, v150
	ds_read2st64_b32 v[68:69], v0 offset0:2 offset1:3
	s_cmp_eq_u32 s67, 4
	s_cselect_b64 s[30:31], -1, 0
	s_and_b64 s[30:31], s[30:31], exec
	s_cselect_b32 s30, s23, s65
	s_waitcnt lgkmcnt(0)
	v_lshl_add_u32 v0, v68, 10, v151
	v_add_u32_e32 v68, s27, v152
	ds_read_b128 v[154:157], v68
	ds_read_b128 v[158:161], v68 offset:1024
	ds_read_b128 v[162:165], v68 offset:2048
	ds_read_b128 v[166:169], v68 offset:3072
	v_add_u32_e32 v68, s43, v152
	s_cselect_b32 s31, s21, s66
	s_add_u32 s68, s28, 0x80
	ds_read_b128 v[170:173], v68
	ds_read_b128 v[174:177], v68 offset:1024
	ds_read_b128 v[186:189], v68 offset:2048
	ds_read_b128 v[190:193], v68 offset:3072
	s_addc_u32 s69, s29, 0
	s_cmp_eq_u32 s67, 4
	s_cselect_b64 s[36:37], -1, 0
	s_and_b64 s[34:35], s[36:37], exec
	s_cselect_b32 s34, s8, s68
	s_cselect_b32 s35, s9, s69
	s_and_b64 s[36:37], s[2:3], s[36:37]
	s_and_b64 s[36:37], s[36:37], exec
	v_lshl_add_u32 v67, v69, 10, v151
	s_cselect_b32 s36, s60, s63
	s_add_i32 m0, s46, 0xc000
	ds_read_b128 v[194:197], v153
	ds_read_b128 v[198:201], v153 offset:1024
	ds_read_b128 v[202:205], v153 offset:2048
	ds_read_b128 v[206:209], v153 offset:3072
	ds_read_b128 v[210:213], v153 offset:4096
	ds_read_b128 v[214:217], v153 offset:5120
	ds_read_b128 v[244:247], v153 offset:6144
	ds_read_b128 v[248:251], v153 offset:7168
	s_nop 0
	global_load_lds_dwordx4 v0, s[28:29]
	s_add_i32 m0, s46, 0xe000
	s_nop 0
	global_load_lds_dwordx4 v67, s[28:29]
	s_waitcnt vmcnt(8)
	s_waitcnt lgkmcnt(0)
	s_barrier
	s_setprio 1
	s_waitcnt lgkmcnt(0)
	s_cmp_eq_u32 s67, -2
	s_cbranch_scc1 .Llzf_1
	v_mfma_f32_16x16x128_f8f6f4 v[142:145], v[154:161], v[194:201], v[142:145]
	v_mfma_f32_16x16x128_f8f6f4 v[134:137], v[162:169], v[194:201], v[134:137]
	v_mfma_f32_16x16x128_f8f6f4 v[126:129], v[154:161], v[202:209], v[126:129]
	v_mfma_f32_16x16x128_f8f6f4 v[118:121], v[162:169], v[202:209], v[118:121]
	v_mfma_f32_16x16x128_f8f6f4 v[110:113], v[154:161], v[210:217], v[110:113]
	v_mfma_f32_16x16x128_f8f6f4 v[102:105], v[162:169], v[210:217], v[102:105]
	v_mfma_f32_16x16x128_f8f6f4 v[178:181], v[154:161], v[244:251], v[94:97]
	v_mfma_f32_16x16x128_f8f6f4 v[182:185], v[162:169], v[244:251], v[78:81]
	s_setprio 0
	s_setprio 1
	v_mfma_f32_16x16x128_f8f6f4 v[138:141], v[170:177], v[194:201], v[138:141]
	v_mfma_f32_16x16x128_f8f6f4 v[130:133], v[186:193], v[194:201], v[130:133]
	v_mfma_f32_16x16x128_f8f6f4 v[122:125], v[170:177], v[202:209], v[122:125]
	v_mfma_f32_16x16x128_f8f6f4 v[114:117], v[186:193], v[202:209], v[114:117]
	v_mfma_f32_16x16x128_f8f6f4 v[106:109], v[170:177], v[210:217], v[106:109]
	v_mfma_f32_16x16x128_f8f6f4 v[194:197], v[186:193], v[210:217], v[98:101]
	v_mfma_f32_16x16x128_f8f6f4 v[198:201], v[170:177], v[244:251], v[86:89]
	v_mfma_f32_16x16x128_f8f6f4 v[202:205], v[186:193], v[244:251], v[70:73]
.Llzj_1:
	s_setprio 0
	s_barrier
	v_lshl_add_u32 v0, s36, 10, v150
	ds_read2st64_b32 v[76:77], v0 offset1:1
	s_nop 2
	ds_read_b128 v[68:71], v153 offset:16384
	ds_read_b128 v[72:75], v153 offset:17408
	v_mov_b32_e32 v101, v148
	s_mov_b32 m0, s41
	s_waitcnt lgkmcnt(0)
	v_lshl_add_u32 v67, v76, 10, v151
	v_lshl_add_u32 v100, v77, 10, v151
	ds_read_b128 v[76:79], v153 offset:18432
	ds_read_b128 v[80:83], v153 offset:19456
	ds_read_b128 v[84:87], v153 offset:20480
	ds_read_b128 v[88:91], v153 offset:21504
	ds_read_b128 v[92:95], v153 offset:22528
	ds_read_b128 v[96:99], v153 offset:23552
	s_add_u32 s36, s30, 0x20000
	global_load_lds_dwordx4 v101, s[30:31]
	v_mov_b32_e32 v101, v149
	s_mov_b32 m0, s42
	s_addc_u32 s37, s31, 0
	global_load_lds_dwordx4 v101, s[30:31]
	v_mov_b32_e32 v101, v148
	s_mov_b32 m0, s44
	s_nop 0
	global_load_lds_dwordx4 v101, s[36:37]
	v_mov_b32_e32 v101, v149
	s_mov_b32 m0, s45
	s_nop 0
	global_load_lds_dwordx4 v101, s[36:37]
	s_mov_b32 m0, s46
	s_nop 0
	global_load_lds_dwordx4 v67, s[34:35]
	s_mov_b32 m0, s47
	s_nop 0
	global_load_lds_dwordx4 v100, s[34:35]
	s_waitcnt vmcnt(8)
	s_waitcnt lgkmcnt(0)
	s_barrier
	s_setprio 1
	v_mfma_f32_16x16x128_f8f6f4 v[62:65], v[154:161], v[68:75], v[62:65]
	v_mfma_f32_16x16x128_f8f6f4 v[54:57], v[162:169], v[68:75], v[54:57]
	s_waitcnt lgkmcnt(0)
	v_mfma_f32_16x16x128_f8f6f4 v[46:49], v[154:161], v[76:83], v[46:49]
	v_mfma_f32_16x16x128_f8f6f4 v[218:221], v[162:169], v[76:83], v[38:41]
	v_mfma_f32_16x16x128_f8f6f4 v[222:225], v[154:161], v[84:91], v[30:33]
	v_mfma_f32_16x16x128_f8f6f4 v[226:229], v[162:169], v[84:91], v[22:25]
	v_mfma_f32_16x16x128_f8f6f4 v[230:233], v[154:161], v[92:99], v[14:17]
	v_mfma_f32_16x16x128_f8f6f4 v[234:237], v[162:169], v[92:99], v[6:9]
	s_setprio 0
	s_setprio 1
	v_mfma_f32_16x16x128_f8f6f4 v[58:61], v[170:177], v[68:75], v[58:61]
	v_mfma_f32_16x16x128_f8f6f4 v[50:53], v[186:193], v[68:75], v[50:53]
	v_mfma_f32_16x16x128_f8f6f4 v[42:45], v[170:177], v[76:83], v[42:45]
	v_mfma_f32_16x16x128_f8f6f4 v[74:77], v[186:193], v[76:83], v[34:37]
	v_mfma_f32_16x16x128_f8f6f4 v[238:241], v[170:177], v[84:91], v[26:29]
	v_mfma_f32_16x16x128_f8f6f4 v[82:85], v[186:193], v[84:91], v[18:21]
	v_mfma_f32_16x16x128_f8f6f4 v[244:247], v[170:177], v[92:99], v[10:13]
	v_mfma_f32_16x16x128_f8f6f4 v[90:93], v[186:193], v[92:99], v[2:5]
	s_setprio 0
	s_barrier
	s_nop 4
	ds_read2st64_b32 v[2:3], v0 offset0:2 offset1:3
	v_add_u32_e32 v10, s52, v152
	s_waitcnt lgkmcnt(0)
	v_lshl_add_u32 v67, v2, 10, v151
	v_lshl_add_u32 v68, v3, 10, v151
	ds_read_b128 v[2:5], v10
	ds_read_b128 v[6:9], v10 offset:1024
	ds_read_b128 v[154:157], v10 offset:2048
	ds_read_b128 v[158:161], v10 offset:3072
	v_add_u32_e32 v10, s57, v152
	ds_read_b128 v[162:165], v10
	ds_read_b128 v[166:169], v10 offset:1024
	ds_read_b128 v[170:173], v10 offset:2048
	ds_read_b128 v[174:177], v10 offset:3072
	s_mov_b32 m0, s48
	ds_read_b128 v[10:13], v153 offset:32768
	ds_read_b128 v[14:17], v153 offset:33792
	ds_read_b128 v[18:21], v153 offset:34816
	ds_read_b128 v[22:25], v153 offset:35840
	ds_read_b128 v[26:29], v153 offset:36864
	ds_read_b128 v[30:33], v153 offset:37888
	ds_read_b128 v[34:37], v153 offset:38912
	ds_read_b128 v[38:41], v153 offset:39936
	s_nop 0
	global_load_lds_dwordx4 v67, s[34:35]
	s_mov_b32 m0, s49
	s_nop 0
	global_load_lds_dwordx4 v68, s[34:35]
	s_waitcnt vmcnt(8)
	s_waitcnt lgkmcnt(0)
	s_barrier
	s_setprio 1
	s_waitcnt lgkmcnt(0)
	v_mfma_f32_16x16x128_f8f6f4 v[142:145], v[2:9], v[10:17], v[142:145]
	v_mfma_f32_16x16x128_f8f6f4 v[134:137], v[154:161], v[10:17], v[134:137]
	v_mfma_f32_16x16x128_f8f6f4 v[126:129], v[2:9], v[18:25], v[126:129]
	v_mfma_f32_16x16x128_f8f6f4 v[118:121], v[154:161], v[18:25], v[118:121]
	v_mfma_f32_16x16x128_f8f6f4 v[110:113], v[2:9], v[26:33], v[110:113]
	v_mfma_f32_16x16x128_f8f6f4 v[102:105], v[154:161], v[26:33], v[102:105]
	v_mfma_f32_16x16x128_f8f6f4 v[94:97], v[2:9], v[34:41], v[178:181]
	v_mfma_f32_16x16x128_f8f6f4 v[78:81], v[154:161], v[34:41], v[182:185]
	s_setprio 0
	s_setprio 1
	v_mfma_f32_16x16x128_f8f6f4 v[138:141], v[162:169], v[10:17], v[138:141]
	v_mfma_f32_16x16x128_f8f6f4 v[130:133], v[170:177], v[10:17], v[130:133]
	v_mfma_f32_16x16x128_f8f6f4 v[122:125], v[162:169], v[18:25], v[122:125]
	v_mfma_f32_16x16x128_f8f6f4 v[114:117], v[170:177], v[18:25], v[114:117]
	v_mfma_f32_16x16x128_f8f6f4 v[106:109], v[162:169], v[26:33], v[106:109]
	v_mfma_f32_16x16x128_f8f6f4 v[98:101], v[170:177], v[26:33], v[194:197]
	v_mfma_f32_16x16x128_f8f6f4 v[86:89], v[162:169], v[34:41], v[198:201]
	v_mfma_f32_16x16x128_f8f6f4 v[70:73], v[170:177], v[34:41], v[202:205]
	s_setprio 0
	s_barrier
	ds_read2st64_b32 v[10:11], v0 offset1:1
	ds_read_b128 v[186:189], v153 offset:49152
	ds_read_b128 v[190:193], v153 offset:50176
	v_mov_b32_e32 v0, v148
	ds_read_b128 v[194:197], v153 offset:51200
	ds_read_b128 v[198:201], v153 offset:52224
	ds_read_b128 v[202:205], v153 offset:53248
	ds_read_b128 v[206:209], v153 offset:54272
	ds_read_b128 v[210:213], v153 offset:55296
	ds_read_b128 v[214:217], v153 offset:56320
	s_mov_b32 m0, s53
	v_lshl_add_u64 v[14:15], s[30:31], 0, v[0:1]
	v_lshl_add_u64 v[14:15], v[14:15], 0, s[82:83]
	v_mov_b32_e32 v0, v149
	global_load_lds_dwordx4 v[14:15], off
	s_mov_b32 m0, s54
	v_lshl_add_u64 v[14:15], s[30:31], 0, v[0:1]
	v_lshl_add_u64 v[14:15], v[14:15], 0, s[82:83]
	s_add_u32 s30, s30, 0x20080
	v_mov_b32_e32 v0, v148
	global_load_lds_dwordx4 v[14:15], off
	s_addc_u32 s31, s31, 0
	s_mov_b32 m0, s58
	s_waitcnt lgkmcnt(0)
	v_lshl_add_u32 v10, v10, 10, v151
	global_load_lds_dwordx4 v0, s[30:31]
	v_mov_b32_e32 v0, v149
	s_mov_b32 m0, s59
	v_lshl_add_u32 v12, v11, 10, v151
	v_mov_b32_e32 v11, v1
	global_load_lds_dwordx4 v0, s[30:31]
	s_mov_b32 m0, s55
	v_lshl_add_u64 v[10:11], s[34:35], 0, v[10:11]
	v_lshl_add_u64 v[10:11], v[10:11], 0, s[82:83]
	v_mov_b32_e32 v13, v1
	global_load_lds_dwordx4 v[10:11], off
	s_mov_b32 m0, s56
	v_lshl_add_u64 v[10:11], s[34:35], 0, v[12:13]
	v_lshl_add_u64 v[10:11], v[10:11], 0, s[82:83]
	global_load_lds_dwordx4 v[10:11], off
	s_waitcnt vmcnt(8)
	s_waitcnt lgkmcnt(0)
	s_barrier
	s_setprio 1
	v_mfma_f32_16x16x128_f8f6f4 v[62:65], v[2:9], v[186:193], v[62:65]
	v_mfma_f32_16x16x128_f8f6f4 v[54:57], v[154:161], v[186:193], v[54:57]
	v_mfma_f32_16x16x128_f8f6f4 v[46:49], v[2:9], v[194:201], v[46:49]
	v_mfma_f32_16x16x128_f8f6f4 v[38:41], v[154:161], v[194:201], v[218:221]
	v_mfma_f32_16x16x128_f8f6f4 v[30:33], v[2:9], v[202:209], v[222:225]
	v_mfma_f32_16x16x128_f8f6f4 v[22:25], v[154:161], v[202:209], v[226:229]
	v_mfma_f32_16x16x128_f8f6f4 v[14:17], v[2:9], v[210:217], v[230:233]
	v_mfma_f32_16x16x128_f8f6f4 v[6:9], v[154:161], v[210:217], v[234:237]
	s_setprio 0
	s_setprio 1
	v_mfma_f32_16x16x128_f8f6f4 v[58:61], v[162:169], v[186:193], v[58:61]
	v_mfma_f32_16x16x128_f8f6f4 v[50:53], v[170:177], v[186:193], v[50:53]
	v_mfma_f32_16x16x128_f8f6f4 v[42:45], v[162:169], v[194:201], v[42:45]
	v_mfma_f32_16x16x128_f8f6f4 v[34:37], v[170:177], v[194:201], v[74:77]
	v_mfma_f32_16x16x128_f8f6f4 v[26:29], v[162:169], v[202:209], v[238:241]
	v_mfma_f32_16x16x128_f8f6f4 v[18:21], v[170:177], v[202:209], v[82:85]
	v_mfma_f32_16x16x128_f8f6f4 v[10:13], v[162:169], v[210:217], v[244:247]
	v_mfma_f32_16x16x128_f8f6f4 v[2:5], v[170:177], v[210:217], v[90:93]
	s_setprio 0
	s_barrier
	s_add_i32 s67, s67, 2
	s_add_u32 s65, s65, 0x100
	s_addc_u32 s66, s66, 0
	s_add_u32 s28, s28, 0x100
	s_addc_u32 s29, s29, 0
	s_cmp_gt_u32 s67, 5
	s_cbranch_scc0 .LBB0_1243
	s_and_b64 vcc, exec, s[16:17]
	s_cbranch_vccz .LBB0_1246
	s_barrier

.LBB0_1348:
	s_ashr_i32 s15, s14, 31
	s_lshl_b64 s[18:19], s[14:15], 18
	s_add_u32 s18, s40, s18
	s_addc_u32 s19, s41, s19
	s_and_b64 s[20:21], s[2:3], exec
	s_cselect_b32 s15, s19, s29
	s_cselect_b32 s64, s18, s28
	s_ashr_i32 s17, s16, 31
	s_lshl_b64 s[20:21], s[16:17], 20
	s_add_u32 s17, s42, s20
	s_addc_u32 s30, s43, s21
	s_ashr_i32 s13, s12, 31
	s_lshl_b64 s[20:21], s[12:13], 18
	s_add_u32 s20, s17, s20
	s_addc_u32 s21, s30, s21
	s_and_b64 s[30:31], s[2:3], exec
	s_cselect_b32 s13, s21, s27
	s_cselect_b32 s17, s20, s26
	s_add_u32 s65, s26, 0x100
	s_addc_u32 s66, s27, 0
	s_add_u32 s26, s28, 0x80
	v_mov_b32_e32 v2, 0
	s_addc_u32 s27, s29, 0
	s_mov_b32 s67, -2
	v_mov_b32_e32 v3, v2
	s_waitcnt vmcnt(0)
	v_mov_b64_e32 v[34:35], v[2:3]
	v_mov_b64_e32 v[36:37], v[2:3]
	v_mov_b64_e32 v[38:39], v[2:3]
	v_mov_b64_e32 v[40:41], v[2:3]
	v_mov_b64_e32 v[42:43], v[2:3]
	v_mov_b64_e32 v[44:45], v[2:3]
	v_mov_b64_e32 v[46:47], v[2:3]
	v_mov_b64_e32 v[48:49], v[2:3]
	v_mov_b64_e32 v[50:51], v[2:3]
	v_mov_b64_e32 v[52:53], v[2:3]
	v_mov_b64_e32 v[54:55], v[2:3]
	v_mov_b64_e32 v[56:57], v[2:3]
	v_mov_b64_e32 v[62:63], v[2:3]
	v_mov_b64_e32 v[64:65], v[2:3]
	v_mov_b64_e32 v[70:71], v[2:3]
	v_mov_b64_e32 v[72:73], v[2:3]
	v_mov_b64_e32 v[98:99], v[2:3]
	v_mov_b64_e32 v[100:101], v[2:3]
	v_mov_b64_e32 v[102:103], v[2:3]
	v_mov_b64_e32 v[104:105], v[2:3]
	v_mov_b64_e32 v[106:107], v[2:3]
	v_mov_b64_e32 v[108:109], v[2:3]
	v_mov_b64_e32 v[110:111], v[2:3]
	v_mov_b64_e32 v[112:113], v[2:3]
	v_mov_b64_e32 v[114:115], v[2:3]
	v_mov_b64_e32 v[116:117], v[2:3]
	v_mov_b64_e32 v[118:119], v[2:3]
	v_mov_b64_e32 v[120:121], v[2:3]
	v_mov_b64_e32 v[122:123], v[2:3]
	v_mov_b64_e32 v[124:125], v[2:3]
	v_mov_b64_e32 v[126:127], v[2:3]
	v_mov_b64_e32 v[128:129], v[2:3]
	s_branch .LBB0_1349
.Llzf_0:
	v_mfma_f32_16x16x128_f8f6f4 v[126:129], v[132:139], v[186:193], v[126:129]
	v_mov_b32_e32 v4, 0
	v_mov_b32_e32 v5, 0
	v_mov_b32_e32 v6, 0
	v_mov_b32_e32 v7, 0
	v_mfma_f32_16x16x128_f8f6f4 v[122:125], v[140:147], v[186:193], v[122:125]
	v_mov_b32_e32 v8, 0
	v_mov_b32_e32 v9, 0
	v_mov_b32_e32 v10, 0
	v_mov_b32_e32 v11, 0
	v_mfma_f32_16x16x128_f8f6f4 v[118:121], v[132:139], v[194:201], v[118:121]
	v_mov_b32_e32 v12, 0
	v_mov_b32_e32 v13, 0
	v_mov_b32_e32 v14, 0
	v_mov_b32_e32 v15, 0
	v_mfma_f32_16x16x128_f8f6f4 v[114:117], v[140:147], v[194:201], v[114:117]
	v_mov_b32_e32 v16, 0
	v_mov_b32_e32 v17, 0
	v_mov_b32_e32 v18, 0
	v_mov_b32_e32 v19, 0
	v_mfma_f32_16x16x128_f8f6f4 v[110:113], v[132:139], v[202:209], v[110:113]
	v_mov_b32_e32 v20, 0
	v_mov_b32_e32 v21, 0
	v_mov_b32_e32 v22, 0
	v_mov_b32_e32 v23, 0
	v_mfma_f32_16x16x128_f8f6f4 v[106:109], v[140:147], v[202:209], v[106:109]
	v_mov_b32_e32 v24, 0
	v_mov_b32_e32 v25, 0
	v_mov_b32_e32 v26, 0
	v_mov_b32_e32 v27, 0
	v_mfma_f32_16x16x128_f8f6f4 v[172:175], v[132:139], v[210:217], v[102:105]
	v_mov_b32_e32 v28, 0
	v_mov_b32_e32 v29, 0
	v_mov_b32_e32 v30, 0
	v_mov_b32_e32 v31, 0
	v_mfma_f32_16x16x128_f8f6f4 v[176:179], v[140:147], v[210:217], v[98:101]
	v_mov_b32_e32 v32, 0
	v_mov_b32_e32 v33, 0
	v_mov_b32_e32 v58, 0
	v_mov_b32_e32 v59, 0
	s_setprio 0
	s_setprio 1
	v_mfma_f32_16x16x128_f8f6f4 v[70:73], v[148:155], v[186:193], v[70:73]
	v_mov_b32_e32 v60, 0
	v_mov_b32_e32 v61, 0
	v_mov_b32_e32 v66, 0
	v_mov_b32_e32 v67, 0
	v_mfma_f32_16x16x128_f8f6f4 v[62:65], v[156:163], v[186:193], v[62:65]
	v_mov_b32_e32 v68, 0
	v_mov_b32_e32 v69, 0
	v_mov_b32_e32 v74, 0
	v_mov_b32_e32 v75, 0
	v_mfma_f32_16x16x128_f8f6f4 v[180:183], v[148:155], v[194:201], v[54:57]
	v_mov_b32_e32 v76, 0
	v_mov_b32_e32 v77, 0
	v_mov_b32_e32 v78, 0
	v_mov_b32_e32 v79, 0
	v_mfma_f32_16x16x128_f8f6f4 v[184:187], v[156:163], v[194:201], v[50:53]
	v_mov_b32_e32 v80, 0
	v_mov_b32_e32 v81, 0
	v_mov_b32_e32 v82, 0
	v_mov_b32_e32 v83, 0
	v_mfma_f32_16x16x128_f8f6f4 v[188:191], v[148:155], v[202:209], v[46:49]
	v_mov_b32_e32 v84, 0
	v_mov_b32_e32 v85, 0
	v_mov_b32_e32 v86, 0
	v_mov_b32_e32 v87, 0
	v_mfma_f32_16x16x128_f8f6f4 v[192:195], v[156:163], v[202:209], v[42:45]
	v_mov_b32_e32 v88, 0
	v_mov_b32_e32 v89, 0
	v_mov_b32_e32 v90, 0
	v_mov_b32_e32 v91, 0
	v_mfma_f32_16x16x128_f8f6f4 v[196:199], v[148:155], v[210:217], v[38:41]
	v_mov_b32_e32 v92, 0
	v_mov_b32_e32 v93, 0
	v_mov_b32_e32 v94, 0
	v_mov_b32_e32 v95, 0
	v_mfma_f32_16x16x128_f8f6f4 v[200:203], v[156:163], v[210:217], v[34:37]
	v_mov_b32_e32 v96, 0
	v_mov_b32_e32 v97, 0
	s_branch .Llzj_0
.LBB0_1349:
	v_add_u32_e32 v0, s23, v170
	ds_read_b128 v[132:135], v0
	ds_read_b128 v[136:139], v0 offset:1024
	ds_read_b128 v[140:143], v0 offset:2048
	ds_read_b128 v[144:147], v0 offset:3072
	v_add_u32_e32 v0, s45, v170
	ds_read_b128 v[148:151], v0
	ds_read_b128 v[152:155], v0 offset:1024
	ds_read_b128 v[156:159], v0 offset:2048
	ds_read_b128 v[160:163], v0 offset:3072
	s_add_u32 s28, s26, 0x80
	s_addc_u32 s29, s27, 0
	s_cmp_eq_u32 s67, 4
	s_cselect_b32 s29, s15, s29
	s_cselect_b32 s28, s64, s28
	s_cselect_b32 s31, s13, s66
	s_cselect_b32 s30, s17, s65
	v_mov_b32_e32 v0, v167
	ds_read_b128 v[186:189], v171
	ds_read_b128 v[190:193], v171 offset:1024
	ds_read_b128 v[194:197], v171 offset:2048
	ds_read_b128 v[198:201], v171 offset:3072
	ds_read_b128 v[202:205], v171 offset:4096
	ds_read_b128 v[206:209], v171 offset:5120
	ds_read_b128 v[210:213], v171 offset:6144
	ds_read_b128 v[214:217], v171 offset:7168
	s_add_i32 m0, s48, 0xc000
	v_add_u32_e32 v0, 0x20000, v0
	global_load_lds_dwordx4 v0, s[26:27]
	v_mov_b32_e32 v0, v169
	s_add_i32 m0, s48, 0xe000
	v_add_u32_e32 v0, 0x20000, v0
	global_load_lds_dwordx4 v0, s[26:27]
	s_waitcnt vmcnt(8)
	s_waitcnt lgkmcnt(0)
	s_barrier
	s_setprio 1
	s_waitcnt lgkmcnt(0)
	s_cmp_eq_u32 s67, -2
	s_cbranch_scc1 .Llzf_0
	v_mfma_f32_16x16x128_f8f6f4 v[126:129], v[132:139], v[186:193], v[126:129]
	v_mfma_f32_16x16x128_f8f6f4 v[122:125], v[140:147], v[186:193], v[122:125]
	v_mfma_f32_16x16x128_f8f6f4 v[118:121], v[132:139], v[194:201], v[118:121]
	v_mfma_f32_16x16x128_f8f6f4 v[114:117], v[140:147], v[194:201], v[114:117]
	v_mfma_f32_16x16x128_f8f6f4 v[110:113], v[132:139], v[202:209], v[110:113]
	v_mfma_f32_16x16x128_f8f6f4 v[106:109], v[140:147], v[202:209], v[106:109]
	v_mfma_f32_16x16x128_f8f6f4 v[172:175], v[132:139], v[210:217], v[102:105]
	v_mfma_f32_16x16x128_f8f6f4 v[176:179], v[140:147], v[210:217], v[98:101]
	s_setprio 0
	s_setprio 1
	v_mfma_f32_16x16x128_f8f6f4 v[70:73], v[148:155], v[186:193], v[70:73]
	v_mfma_f32_16x16x128_f8f6f4 v[62:65], v[156:163], v[186:193], v[62:65]
	v_mfma_f32_16x16x128_f8f6f4 v[180:183], v[148:155], v[194:201], v[54:57]
	v_mfma_f32_16x16x128_f8f6f4 v[184:187], v[156:163], v[194:201], v[50:53]
	v_mfma_f32_16x16x128_f8f6f4 v[188:191], v[148:155], v[202:209], v[46:49]
	v_mfma_f32_16x16x128_f8f6f4 v[192:195], v[156:163], v[202:209], v[42:45]
	v_mfma_f32_16x16x128_f8f6f4 v[196:199], v[148:155], v[210:217], v[38:41]
	v_mfma_f32_16x16x128_f8f6f4 v[200:203], v[156:163], v[210:217], v[34:37]
.Llzj_0:
	s_setprio 0
	s_barrier
	v_mov_b32_e32 v0, v166
	s_mov_b32 m0, s25
	s_nop 2
	ds_read_b128 v[34:37], v171 offset:16384
	ds_read_b128 v[38:41], v171 offset:17408
	ds_read_b128 v[42:45], v171 offset:18432
	ds_read_b128 v[46:49], v171 offset:19456
	ds_read_b128 v[50:53], v171 offset:20480
	ds_read_b128 v[54:57], v171 offset:21504
	ds_read_b128 v[98:101], v171 offset:22528
	ds_read_b128 v[102:105], v171 offset:23552
	s_add_u32 s68, s30, 0x20000
	global_load_lds_dwordx4 v0, s[30:31]
	v_mov_b32_e32 v0, v168
	s_mov_b32 m0, s44
	s_addc_u32 s69, s31, 0
	global_load_lds_dwordx4 v0, s[30:31]
	v_mov_b32_e32 v0, v166
	s_mov_b32 m0, s46
	s_nop 0
	global_load_lds_dwordx4 v0, s[68:69]
	v_mov_b32_e32 v0, v168
	s_mov_b32 m0, s47
	s_nop 0
	global_load_lds_dwordx4 v0, s[68:69]
	v_mov_b32_e32 v0, v167
	s_mov_b32 m0, s48
	s_nop 0
	global_load_lds_dwordx4 v0, s[28:29]
	v_mov_b32_e32 v0, v169
	s_mov_b32 m0, s49
	s_nop 0
	global_load_lds_dwordx4 v0, s[28:29]
	s_waitcnt vmcnt(8)
	s_waitcnt lgkmcnt(0)
	s_barrier
	s_setprio 1
	s_waitcnt lgkmcnt(0)
	v_mfma_f32_16x16x128_f8f6f4 v[94:97], v[132:139], v[34:41], v[94:97]
	v_mfma_f32_16x16x128_f8f6f4 v[90:93], v[140:147], v[34:41], v[90:93]
	v_mfma_f32_16x16x128_f8f6f4 v[86:89], v[132:139], v[42:49], v[86:89]
	v_mfma_f32_16x16x128_f8f6f4 v[82:85], v[140:147], v[42:49], v[82:85]
	v_mfma_f32_16x16x128_f8f6f4 v[66:69], v[132:139], v[98:105], v[66:69]
	v_mfma_f32_16x16x128_f8f6f4 v[58:61], v[140:147], v[98:105], v[58:61]
	v_mfma_f32_16x16x128_f8f6f4 v[204:207], v[132:139], v[50:57], v[78:81]
	v_mfma_f32_16x16x128_f8f6f4 v[208:211], v[140:147], v[50:57], v[74:77]
	s_setprio 0
	s_setprio 1
	v_mfma_f32_16x16x128_f8f6f4 v[212:215], v[148:155], v[34:41], v[30:33]
	v_mfma_f32_16x16x128_f8f6f4 v[216:219], v[156:163], v[34:41], v[26:29]
	v_mfma_f32_16x16x128_f8f6f4 v[220:223], v[148:155], v[42:49], v[22:25]
	v_mfma_f32_16x16x128_f8f6f4 v[224:227], v[156:163], v[42:49], v[18:21]
	v_mfma_f32_16x16x128_f8f6f4 v[228:231], v[148:155], v[50:57], v[14:17]
	v_mfma_f32_16x16x128_f8f6f4 v[232:235], v[156:163], v[50:57], v[10:13]
	v_mfma_f32_16x16x128_f8f6f4 v[236:239], v[148:155], v[98:105], v[6:9]
	v_mfma_f32_16x16x128_f8f6f4 v[244:247], v[156:163], v[98:105], v[2:5]
	s_setprio 0
	s_barrier
	v_add_u32_e32 v0, s54, v170
	s_nop 3
	ds_read_b128 v[2:5], v0
	ds_read_b128 v[6:9], v0 offset:1024
	ds_read_b128 v[10:13], v0 offset:2048
	ds_read_b128 v[14:17], v0 offset:3072
	v_add_u32_e32 v0, s59, v170
	ds_read_b128 v[132:135], v0
	ds_read_b128 v[136:139], v0 offset:1024
	ds_read_b128 v[140:143], v0 offset:2048
	ds_read_b128 v[144:147], v0 offset:3072
	v_mov_b32_e32 v0, v167
	ds_read_b128 v[18:21], v171 offset:32768
	ds_read_b128 v[22:25], v171 offset:33792
	ds_read_b128 v[26:29], v171 offset:34816
	ds_read_b128 v[30:33], v171 offset:35840
	ds_read_b128 v[34:37], v171 offset:36864
	ds_read_b128 v[38:41], v171 offset:37888
	ds_read_b128 v[74:77], v171 offset:38912
	ds_read_b128 v[78:81], v171 offset:39936
	s_mov_b32 m0, s50
	v_add_u32_e32 v0, 0x20000, v0
	global_load_lds_dwordx4 v0, s[28:29]
	v_mov_b32_e32 v0, v169
	s_mov_b32 m0, s51
	v_add_u32_e32 v0, 0x20000, v0
	global_load_lds_dwordx4 v0, s[28:29]
	s_waitcnt vmcnt(8)
	s_waitcnt lgkmcnt(0)
	s_barrier
	s_setprio 1
	s_waitcnt lgkmcnt(0)
	v_mfma_f32_16x16x128_f8f6f4 v[126:129], v[2:9], v[18:25], v[126:129]
	v_mfma_f32_16x16x128_f8f6f4 v[122:125], v[10:17], v[18:25], v[122:125]
	v_mfma_f32_16x16x128_f8f6f4 v[118:121], v[2:9], v[26:33], v[118:121]
	v_mfma_f32_16x16x128_f8f6f4 v[114:117], v[10:17], v[26:33], v[114:117]
	v_mfma_f32_16x16x128_f8f6f4 v[110:113], v[2:9], v[34:41], v[110:113]
	v_mfma_f32_16x16x128_f8f6f4 v[106:109], v[10:17], v[34:41], v[106:109]
	v_mfma_f32_16x16x128_f8f6f4 v[102:105], v[2:9], v[74:81], v[172:175]
	v_mfma_f32_16x16x128_f8f6f4 v[98:101], v[10:17], v[74:81], v[176:179]
	s_setprio 0
	s_setprio 1
	v_mfma_f32_16x16x128_f8f6f4 v[70:73], v[132:139], v[18:25], v[70:73]
	v_mfma_f32_16x16x128_f8f6f4 v[62:65], v[140:147], v[18:25], v[62:65]
	v_mfma_f32_16x16x128_f8f6f4 v[54:57], v[132:139], v[26:33], v[180:183]
	v_mfma_f32_16x16x128_f8f6f4 v[50:53], v[140:147], v[26:33], v[184:187]
	v_mfma_f32_16x16x128_f8f6f4 v[46:49], v[132:139], v[34:41], v[188:191]
	v_mfma_f32_16x16x128_f8f6f4 v[42:45], v[140:147], v[34:41], v[192:195]
	v_mfma_f32_16x16x128_f8f6f4 v[38:41], v[132:139], v[74:81], v[196:199]
	v_mfma_f32_16x16x128_f8f6f4 v[34:37], v[140:147], v[74:81], v[200:203]
	s_setprio 0
	s_barrier
	v_mov_b32_e32 v0, v166
	ds_read_b128 v[18:21], v171 offset:49152
	ds_read_b128 v[22:25], v171 offset:50176
	ds_read_b128 v[148:151], v171 offset:51200
	ds_read_b128 v[152:155], v171 offset:52224
	ds_read_b128 v[156:159], v171 offset:53248
	ds_read_b128 v[160:163], v171 offset:54272
	ds_read_b128 v[186:189], v171 offset:55296
	ds_read_b128 v[190:193], v171 offset:56320
	s_mov_b32 m0, s55
	v_lshl_add_u64 v[26:27], s[30:31], 0, v[0:1]
	v_lshl_add_u64 v[26:27], v[26:27], 0, s[82:83]
	v_mov_b32_e32 v0, v168
	global_load_lds_dwordx4 v[26:27], off
	s_mov_b32 m0, s56
	v_lshl_add_u64 v[26:27], s[30:31], 0, v[0:1]
	v_lshl_add_u64 v[26:27], v[26:27], 0, s[82:83]
	s_add_u32 s30, s30, 0x20080
	v_mov_b32_e32 v0, v166
	global_load_lds_dwordx4 v[26:27], off
	s_addc_u32 s31, s31, 0
	s_mov_b32 m0, s60
	s_nop 0
	global_load_lds_dwordx4 v0, s[30:31]
	v_mov_b32_e32 v0, v168
	s_mov_b32 m0, s61
	s_nop 0
	global_load_lds_dwordx4 v0, s[30:31]
	v_mov_b32_e32 v0, v167
	s_mov_b32 m0, s57
	v_lshl_add_u64 v[26:27], s[28:29], 0, v[0:1]
	v_lshl_add_u64 v[26:27], v[26:27], 0, s[82:83]
	v_mov_b32_e32 v0, v169
	global_load_lds_dwordx4 v[26:27], off
	s_mov_b32 m0, s58
	v_lshl_add_u64 v[26:27], s[28:29], 0, v[0:1]
	v_lshl_add_u64 v[26:27], v[26:27], 0, s[82:83]
	global_load_lds_dwordx4 v[26:27], off
	s_waitcnt vmcnt(8)
	s_waitcnt lgkmcnt(0)
	s_barrier
	s_setprio 1
	s_waitcnt lgkmcnt(0)
	v_mfma_f32_16x16x128_f8f6f4 v[94:97], v[2:9], v[18:25], v[94:97]
	v_mfma_f32_16x16x128_f8f6f4 v[90:93], v[10:17], v[18:25], v[90:93]
	v_mfma_f32_16x16x128_f8f6f4 v[86:89], v[2:9], v[148:155], v[86:89]
	v_mfma_f32_16x16x128_f8f6f4 v[82:85], v[10:17], v[148:155], v[82:85]
	v_mfma_f32_16x16x128_f8f6f4 v[78:81], v[2:9], v[156:163], v[204:207]
	v_mfma_f32_16x16x128_f8f6f4 v[74:77], v[10:17], v[156:163], v[208:211]
	v_mfma_f32_16x16x128_f8f6f4 v[66:69], v[2:9], v[186:193], v[66:69]
	v_mfma_f32_16x16x128_f8f6f4 v[58:61], v[10:17], v[186:193], v[58:61]
	s_setprio 0
	s_setprio 1
	v_mfma_f32_16x16x128_f8f6f4 v[30:33], v[132:139], v[18:25], v[212:215]
	v_mfma_f32_16x16x128_f8f6f4 v[26:29], v[140:147], v[18:25], v[216:219]
	v_mfma_f32_16x16x128_f8f6f4 v[22:25], v[132:139], v[148:155], v[220:223]
	v_mfma_f32_16x16x128_f8f6f4 v[18:21], v[140:147], v[148:155], v[224:227]
	v_mfma_f32_16x16x128_f8f6f4 v[14:17], v[132:139], v[156:163], v[228:231]
	v_mfma_f32_16x16x128_f8f6f4 v[10:13], v[140:147], v[156:163], v[232:235]
	v_mfma_f32_16x16x128_f8f6f4 v[6:9], v[132:139], v[186:193], v[236:239]
	v_mfma_f32_16x16x128_f8f6f4 v[2:5], v[140:147], v[186:193], v[244:247]
	s_setprio 0
	s_barrier
	s_add_i32 s67, s67, 2
	s_add_u32 s65, s65, 0x100
	s_addc_u32 s66, s66, 0
	s_add_u32 s26, s26, 0x100
	s_addc_u32 s27, s27, 0
	s_cmp_gt_u32 s67, 5
	s_cbranch_scc0 .LBB0_1349
	s_and_b64 vcc, exec, s[8:9]
	s_cbranch_vccz .LBB0_1352
	s_barrier
